# v16 + LDS-DMA pieces 2..4 of each K tile spread over MFMA groups 1-2 instead of bunched at the tile head
# speedup vs baseline: 1.0334x; 1.0031x over previous
; #define G_ENDTILE(VM) do { asm volatile("s_waitcnt vmcnt(" #VM ")" ::: "memory"); \
;         asm volatile("s_waitcnt lgkmcnt(0)" ::: "memory"); __builtin_amdgcn_s_barrier(); asm volatile("" ::: "memory"); } while (0)
;     ...
;         for (int t = 0; t < nt - 2; t += 2) {
;             G_TILE(G_A0, G_B0, true, G_B1, G_A1, t + 1, true, t + 2, (void)0);
;             G_ENDTILE(8);
.LBB0_71:
	s_mov_b32 m0, s68
	s_add_i32 s25, s24, 0xffffff80
	ds_read_b64_tr_b16 v[170:171], v166
	ds_read_b64_tr_b16 v[172:173], v167
	ds_read_b64_tr_b16 v[176:177], v167 offset:32
	ds_read_b128 v[178:181], v162
	ds_read_b64_tr_b16 v[174:175], v166 offset:32
	ds_read_b64_tr_b16 v[182:183], v166 offset:64
	ds_read_b64_tr_b16 v[186:187], v166 offset:96
	ds_read_b64_tr_b16 v[184:185], v167 offset:64
	ds_read_b64_tr_b16 v[188:189], v167 offset:96
	ds_read_b128 v[190:193], v162 offset:2048
	ds_read_b128 v[194:197], v162 offset:4096
	buffer_load_dwordx4 v163, s[20:23], s25 offen lds
	s_mov_b32 m0, s67
	v_mfma_f32_16x16x32_bf16 v[44:47], v[244:247], v[252:255], v[44:47]
	v_mfma_f32_16x16x32_bf16 v[40:43], v[248:251], v[252:255], v[40:43]
	v_mfma_f32_16x16x32_bf16 v[36:39], v[198:201], v[252:255], v[36:39]
	v_mfma_f32_16x16x32_bf16 v[32:35], v[202:205], v[252:255], v[32:35]
	s_waitcnt lgkmcnt(7)
	v_mfma_f32_16x16x32_bf16 v[156:159], v[170:173], v[178:181], v[156:159]
	buffer_load_dwordx4 v165, s[20:23], s25 offen lds
	s_waitcnt lgkmcnt(6)
	v_mfma_f32_16x16x32_bf16 v[152:155], v[174:177], v[178:181], v[152:155]
	s_waitcnt lgkmcnt(3)
	v_mfma_f32_16x16x32_bf16 v[148:151], v[182:185], v[178:181], v[148:151]
	s_waitcnt lgkmcnt(2)
	v_mfma_f32_16x16x32_bf16 v[144:147], v[186:189], v[178:181], v[144:147]
	s_waitcnt lgkmcnt(1)
	v_mfma_f32_16x16x32_bf16 v[140:143], v[170:173], v[190:193], v[140:143]
	s_mov_b32 m0, s66
	s_nop 0
	buffer_load_dwordx4 v164, s[20:23], s25 offen lds
	ds_read_b128 v[178:181], v162 offset:6144
	s_waitcnt vmcnt(10)
	v_cvt_pk_bf16_f32 v15, v14, v15
	v_cvt_pk_bf16_f32 v14, v12, v13
	v_mfma_f32_16x16x32_bf16 v[136:139], v[174:177], v[190:193], v[136:139]
	ds_write_b64 v161, v[14:15] offset:34816
	v_mfma_f32_16x16x32_bf16 v[132:135], v[182:185], v[190:193], v[132:135]
	s_mov_b32 m0, s65
	s_nop 0
	buffer_load_dwordx4 v168, s[20:23], s25 offen lds
	s_add_i32 s25, s9, 0xffd60000
	v_mfma_f32_16x16x32_bf16 v[128:131], v[186:189], v[190:193], v[128:131]
	s_waitcnt lgkmcnt(2)
	v_mfma_f32_16x16x32_bf16 v[124:127], v[170:173], v[194:197], v[124:127]
	ds_read_b128 v[190:193], v162 offset:8192
	v_mfma_f32_16x16x32_bf16 v[120:123], v[174:177], v[194:197], v[120:123]
	v_mfma_f32_16x16x32_bf16 v[116:119], v[182:185], v[194:197], v[116:119]
	v_mfma_f32_16x16x32_bf16 v[112:115], v[186:189], v[194:197], v[112:115]
	s_waitcnt lgkmcnt(2)
	v_mfma_f32_16x16x32_bf16 v[108:111], v[170:173], v[178:181], v[108:111]
	ds_read_b128 v[194:197], v162 offset:10240
	buffer_load_dwordx4 v[12:15], v160, s[12:15], s25 offen
	s_waitcnt vmcnt(11)
	v_cvt_pk_bf16_f32 v3, v2, v3
	v_cvt_pk_bf16_f32 v2, v0, v1
	v_mfma_f32_16x16x32_bf16 v[104:107], v[174:177], v[178:181], v[104:107]
	ds_write_b64 v161, v[2:3] offset:43520
	v_mfma_f32_16x16x32_bf16 v[100:103], v[182:185], v[178:181], v[100:103]
	v_mfma_f32_16x16x32_bf16 v[96:99], v[186:189], v[178:181], v[96:99]
	s_add_i32 s26, s9, 0xffdc0000
	s_waitcnt lgkmcnt(2)
	v_mfma_f32_16x16x32_bf16 v[92:95], v[170:173], v[190:193], v[92:95]
	ds_read_b128 v[178:181], v162 offset:12288
	v_mfma_f32_16x16x32_bf16 v[88:91], v[174:177], v[190:193], v[88:91]
	v_mfma_f32_16x16x32_bf16 v[84:87], v[182:185], v[190:193], v[84:87]
	v_mfma_f32_16x16x32_bf16 v[80:83], v[186:189], v[190:193], v[80:83]
	s_waitcnt lgkmcnt(2)
	v_mfma_f32_16x16x32_bf16 v[76:79], v[170:173], v[194:197], v[76:79]
	ds_read_b128 v[190:193], v162 offset:14336
	buffer_load_dwordx4 v[0:3], v160, s[12:15], s26 offen
	s_waitcnt vmcnt(11)
	v_cvt_pk_bf16_f32 v31, v30, v31
	v_cvt_pk_bf16_f32 v30, v28, v29
	v_mfma_f32_16x16x32_bf16 v[72:75], v[174:177], v[194:197], v[72:75]
	ds_write_b64 v161, v[30:31] offset:52224
	v_mfma_f32_16x16x32_bf16 v[68:71], v[182:185], v[194:197], v[68:71]
	v_mfma_f32_16x16x32_bf16 v[64:67], v[186:189], v[194:197], v[64:67]
	s_add_i32 s27, s9, 0xffe20000
	s_waitcnt lgkmcnt(2)
	v_mfma_f32_16x16x32_bf16 v[60:63], v[170:173], v[178:181], v[60:63]
	ds_read_b128 v[194:197], v162 offset:1024
	v_mfma_f32_16x16x32_bf16 v[56:59], v[174:177], v[178:181], v[56:59]
	v_mfma_f32_16x16x32_bf16 v[52:55], v[182:185], v[178:181], v[52:55]
	v_mfma_f32_16x16x32_bf16 v[48:51], v[186:189], v[178:181], v[48:51]
	s_waitcnt lgkmcnt(2)
	v_mfma_f32_16x16x32_bf16 v[44:47], v[170:173], v[190:193], v[44:47]
	ds_read_b128 v[170:173], v162 offset:3072
	buffer_load_dwordx4 v[28:31], v160, s[12:15], s27 offen
	s_waitcnt vmcnt(11)
	v_cvt_pk_bf16_f32 v27, v26, v27
	v_cvt_pk_bf16_f32 v26, v24, v25
	v_mfma_f32_16x16x32_bf16 v[40:43], v[174:177], v[190:193], v[40:43]
	ds_read_b64_tr_b16 v[244:245], v166 offset:17408
	ds_read_b64_tr_b16 v[248:249], v166 offset:17440
	ds_read_b64_tr_b16 v[198:199], v166 offset:17472
	ds_read_b64_tr_b16 v[202:203], v166 offset:17504
	ds_read_b64_tr_b16 v[246:247], v167 offset:17408
	ds_read_b64_tr_b16 v[250:251], v167 offset:17440
	ds_read_b64_tr_b16 v[200:201], v167 offset:17472
	ds_read_b64_tr_b16 v[204:205], v167 offset:17504
	ds_write_b64 v161, v[26:27] offset:60928
	v_mfma_f32_16x16x32_bf16 v[36:39], v[182:185], v[190:193], v[36:39]
	v_mfma_f32_16x16x32_bf16 v[32:35], v[186:189], v[190:193], v[32:35]
	s_add_i32 s42, s9, 0xffe80000
	s_waitcnt lgkmcnt(4)
	v_mfma_f32_16x16x32_bf16 v[156:159], v[244:247], v[194:197], v[156:159]
	ds_read_b128 v[182:185], v162 offset:5120
	s_waitcnt lgkmcnt(4)
	v_mfma_f32_16x16x32_bf16 v[152:155], v[248:251], v[194:197], v[152:155]
	s_waitcnt lgkmcnt(3)
	v_mfma_f32_16x16x32_bf16 v[148:151], v[198:201], v[194:197], v[148:151]
	s_waitcnt lgkmcnt(2)
	v_mfma_f32_16x16x32_bf16 v[144:147], v[202:205], v[194:197], v[144:147]
	v_mfma_f32_16x16x32_bf16 v[140:143], v[244:247], v[170:173], v[140:143]
	ds_read_b128 v[186:189], v162 offset:7168
	buffer_load_dwordx4 v[24:27], v160, s[12:15], s42 offen
	s_waitcnt vmcnt(11)
; #define G_ENDTILE(VM) do { asm volatile("s_waitcnt vmcnt(" #VM ")" ::: "memory"); \
;         asm volatile("s_waitcnt lgkmcnt(0)" ::: "memory"); __builtin_amdgcn_s_barrier(); asm volatile("" ::: "memory"); } while (0)
;     ...
;         for (int t = 0; t < nt - 2; t += 2) {
;             G_TILE(G_A0, G_B0, true, G_B1, G_A1, t + 1, true, t + 2, (void)0);
;             G_ENDTILE(8);
;             G_TILE(G_A1, G_B1, true, G_B0, G_A0, t + 2, true, t + 3, (void)0);
;             G_ENDTILE(8);
	v_cvt_pk_bf16_f32 v23, v22, v23
	v_cvt_pk_bf16_f32 v22, v20, v21
	v_mfma_f32_16x16x32_bf16 v[136:139], v[248:251], v[170:173], v[136:139]
	ds_write_b64 v161, v[22:23] offset:35072
	v_mfma_f32_16x16x32_bf16 v[132:135], v[198:201], v[170:173], v[132:135]
	v_mfma_f32_16x16x32_bf16 v[128:131], v[202:205], v[170:173], v[128:131]
	s_waitcnt lgkmcnt(2)
	v_mfma_f32_16x16x32_bf16 v[124:127], v[244:247], v[182:185], v[124:127]
	ds_read_b128 v[170:173], v162 offset:9216
	v_mfma_f32_16x16x32_bf16 v[120:123], v[248:251], v[182:185], v[120:123]
	v_mfma_f32_16x16x32_bf16 v[116:119], v[198:201], v[182:185], v[116:119]
	v_mfma_f32_16x16x32_bf16 v[112:115], v[202:205], v[182:185], v[112:115]
	s_waitcnt lgkmcnt(2)
	v_mfma_f32_16x16x32_bf16 v[108:111], v[244:247], v[186:189], v[108:111]
	ds_read_b128 v[182:185], v162 offset:11264
	buffer_load_dwordx4 v[20:23], v160, s[16:19], s25 offen
	s_waitcnt vmcnt(11)
	v_cvt_pk_bf16_f32 v7, v6, v7
	v_cvt_pk_bf16_f32 v6, v4, v5
	v_mfma_f32_16x16x32_bf16 v[104:107], v[248:251], v[186:189], v[104:107]
	ds_write_b64 v161, v[6:7] offset:43776
	v_mfma_f32_16x16x32_bf16 v[100:103], v[198:201], v[186:189], v[100:103]
	v_mfma_f32_16x16x32_bf16 v[96:99], v[202:205], v[186:189], v[96:99]
	s_waitcnt lgkmcnt(2)
	v_mfma_f32_16x16x32_bf16 v[92:95], v[244:247], v[170:173], v[92:95]
	ds_read_b128 v[186:189], v162 offset:13312
	v_mfma_f32_16x16x32_bf16 v[88:91], v[248:251], v[170:173], v[88:91]
	v_mfma_f32_16x16x32_bf16 v[84:87], v[198:201], v[170:173], v[84:87]
	v_mfma_f32_16x16x32_bf16 v[80:83], v[202:205], v[170:173], v[80:83]
	s_waitcnt lgkmcnt(2)
	v_mfma_f32_16x16x32_bf16 v[76:79], v[244:247], v[182:185], v[76:79]
	ds_read_b128 v[252:255], v162 offset:15360
	buffer_load_dwordx4 v[4:7], v160, s[16:19], s26 offen
	s_waitcnt vmcnt(11)
	v_cvt_pk_bf16_f32 v11, v10, v11
	v_cvt_pk_bf16_f32 v10, v8, v9
	v_mfma_f32_16x16x32_bf16 v[72:75], v[248:251], v[182:185], v[72:75]
	ds_write_b64 v161, v[10:11] offset:52480
	v_mfma_f32_16x16x32_bf16 v[68:71], v[198:201], v[182:185], v[68:71]
	v_mfma_f32_16x16x32_bf16 v[64:67], v[202:205], v[182:185], v[64:67]
	s_waitcnt lgkmcnt(2)
	v_mfma_f32_16x16x32_bf16 v[60:63], v[244:247], v[186:189], v[60:63]
	v_mfma_f32_16x16x32_bf16 v[56:59], v[248:251], v[186:189], v[56:59]
	v_mfma_f32_16x16x32_bf16 v[52:55], v[198:201], v[186:189], v[52:55]
	v_mfma_f32_16x16x32_bf16 v[48:51], v[202:205], v[186:189], v[48:51]
	s_waitcnt lgkmcnt(1)
	buffer_load_dwordx4 v[8:11], v160, s[16:19], s27 offen
	s_waitcnt vmcnt(11)
	v_cvt_pk_bf16_f32 v19, v18, v19
	v_cvt_pk_bf16_f32 v18, v16, v17
	ds_write_b64 v161, v[18:19] offset:61184
	buffer_load_dwordx4 v[16:19], v160, s[16:19], s42 offen
	s_waitcnt vmcnt(8)
	s_mov_b32 m0, s55
	s_waitcnt lgkmcnt(0)
	s_barrier
	ds_read_b64_tr_b16 v[170:171], v166 offset:34816
	ds_read_b64_tr_b16 v[172:173], v167 offset:34816
	ds_read_b64_tr_b16 v[176:177], v167 offset:34848
	ds_read_b128 v[178:181], v162 offset:32768
	ds_read_b64_tr_b16 v[174:175], v166 offset:34848
	ds_read_b64_tr_b16 v[182:183], v166 offset:34880
	ds_read_b64_tr_b16 v[186:187], v166 offset:34912
	ds_read_b64_tr_b16 v[184:185], v167 offset:34880
	ds_read_b64_tr_b16 v[188:189], v167 offset:34912
	ds_read_b128 v[190:193], v162 offset:34816
	ds_read_b128 v[194:197], v162 offset:36864
	buffer_load_dwordx4 v163, s[20:23], s24 offen lds
	s_mov_b32 m0, s56
	v_mfma_f32_16x16x32_bf16 v[44:47], v[244:247], v[252:255], v[44:47]
	v_mfma_f32_16x16x32_bf16 v[40:43], v[248:251], v[252:255], v[40:43]
	v_mfma_f32_16x16x32_bf16 v[36:39], v[198:201], v[252:255], v[36:39]
	v_mfma_f32_16x16x32_bf16 v[32:35], v[202:205], v[252:255], v[32:35]
	s_waitcnt lgkmcnt(7)
	v_mfma_f32_16x16x32_bf16 v[156:159], v[170:173], v[178:181], v[156:159]
	buffer_load_dwordx4 v165, s[20:23], s24 offen lds
	s_add_i32 s25, s9, 0xffee0000
	s_waitcnt lgkmcnt(6)
	v_mfma_f32_16x16x32_bf16 v[152:155], v[174:177], v[178:181], v[152:155]
	s_waitcnt lgkmcnt(3)
	v_mfma_f32_16x16x32_bf16 v[148:151], v[182:185], v[178:181], v[148:151]
	s_waitcnt lgkmcnt(2)
	v_mfma_f32_16x16x32_bf16 v[144:147], v[186:189], v[178:181], v[144:147]
	s_waitcnt lgkmcnt(1)
	v_mfma_f32_16x16x32_bf16 v[140:143], v[170:173], v[190:193], v[140:143]
	s_mov_b32 m0, s57
	s_nop 0
	buffer_load_dwordx4 v164, s[20:23], s24 offen lds
	ds_read_b128 v[178:181], v162 offset:38912
	s_waitcnt vmcnt(10)
	v_cvt_pk_bf16_f32 v15, v14, v15
	v_cvt_pk_bf16_f32 v14, v12, v13
	v_mfma_f32_16x16x32_bf16 v[136:139], v[174:177], v[190:193], v[136:139]
	ds_write_b64 v161, v[14:15]
	v_mfma_f32_16x16x32_bf16 v[132:135], v[182:185], v[190:193], v[132:135]
	s_mov_b32 m0, s59
	s_nop 0
	buffer_load_dwordx4 v168, s[20:23], s24 offen lds
	v_mfma_f32_16x16x32_bf16 v[128:131], v[186:189], v[190:193], v[128:131]
	s_waitcnt lgkmcnt(2)
	v_mfma_f32_16x16x32_bf16 v[124:127], v[170:173], v[194:197], v[124:127]
	ds_read_b128 v[190:193], v162 offset:40960
	v_mfma_f32_16x16x32_bf16 v[120:123], v[174:177], v[194:197], v[120:123]
	v_mfma_f32_16x16x32_bf16 v[116:119], v[182:185], v[194:197], v[116:119]
	v_mfma_f32_16x16x32_bf16 v[112:115], v[186:189], v[194:197], v[112:115]
	s_waitcnt lgkmcnt(2)
	v_mfma_f32_16x16x32_bf16 v[108:111], v[170:173], v[178:181], v[108:111]
	ds_read_b128 v[194:197], v162 offset:43008
	buffer_load_dwordx4 v[12:15], v160, s[12:15], s25 offen
	s_waitcnt vmcnt(11)
	v_cvt_pk_bf16_f32 v3, v2, v3
	v_cvt_pk_bf16_f32 v2, v0, v1
	v_mfma_f32_16x16x32_bf16 v[104:107], v[174:177], v[178:181], v[104:107]
	ds_write_b64 v161, v[2:3] offset:8704
	v_mfma_f32_16x16x32_bf16 v[100:103], v[182:185], v[178:181], v[100:103]
	v_mfma_f32_16x16x32_bf16 v[96:99], v[186:189], v[178:181], v[96:99]
	s_add_i32 s26, s9, 0xfff40000
	s_waitcnt lgkmcnt(2)
; #define G_ENDTILE(VM) do { asm volatile("s_waitcnt vmcnt(" #VM ")" ::: "memory"); \
;         asm volatile("s_waitcnt lgkmcnt(0)" ::: "memory"); __builtin_amdgcn_s_barrier(); asm volatile("" ::: "memory"); } while (0)
;     ...
;         for (int t = 0; t < nt - 2; t += 2) {
;             G_TILE(G_A0, G_B0, true, G_B1, G_A1, t + 1, true, t + 2, (void)0);
;             G_ENDTILE(8);
;             G_TILE(G_A1, G_B1, true, G_B0, G_A0, t + 2, true, t + 3, (void)0);
;             G_ENDTILE(8);
;         }
	v_mfma_f32_16x16x32_bf16 v[92:95], v[170:173], v[190:193], v[92:95]
	ds_read_b128 v[178:181], v162 offset:45056
	v_mfma_f32_16x16x32_bf16 v[88:91], v[174:177], v[190:193], v[88:91]
	v_mfma_f32_16x16x32_bf16 v[84:87], v[182:185], v[190:193], v[84:87]
	v_mfma_f32_16x16x32_bf16 v[80:83], v[186:189], v[190:193], v[80:83]
	s_waitcnt lgkmcnt(2)
	v_mfma_f32_16x16x32_bf16 v[76:79], v[170:173], v[194:197], v[76:79]
	ds_read_b128 v[190:193], v162 offset:47104
	buffer_load_dwordx4 v[0:3], v160, s[12:15], s26 offen
	s_waitcnt vmcnt(11)
	v_cvt_pk_bf16_f32 v31, v30, v31
	v_cvt_pk_bf16_f32 v30, v28, v29
	v_mfma_f32_16x16x32_bf16 v[72:75], v[174:177], v[194:197], v[72:75]
	ds_write_b64 v161, v[30:31] offset:17408
	v_mfma_f32_16x16x32_bf16 v[68:71], v[182:185], v[194:197], v[68:71]
	v_mfma_f32_16x16x32_bf16 v[64:67], v[186:189], v[194:197], v[64:67]
	s_add_i32 s27, s9, 0xfffa0000
	s_waitcnt lgkmcnt(2)
	v_mfma_f32_16x16x32_bf16 v[60:63], v[170:173], v[178:181], v[60:63]
	ds_read_b128 v[194:197], v162 offset:33792
	v_mfma_f32_16x16x32_bf16 v[56:59], v[174:177], v[178:181], v[56:59]
	v_mfma_f32_16x16x32_bf16 v[52:55], v[182:185], v[178:181], v[52:55]
	v_mfma_f32_16x16x32_bf16 v[48:51], v[186:189], v[178:181], v[48:51]
	s_waitcnt lgkmcnt(2)
	v_mfma_f32_16x16x32_bf16 v[44:47], v[170:173], v[190:193], v[44:47]
	ds_read_b128 v[170:173], v162 offset:35840
	buffer_load_dwordx4 v[28:31], v160, s[12:15], s27 offen
	s_waitcnt vmcnt(11)
	v_cvt_pk_bf16_f32 v27, v26, v27
	v_cvt_pk_bf16_f32 v26, v24, v25
	v_mfma_f32_16x16x32_bf16 v[40:43], v[174:177], v[190:193], v[40:43]
	ds_read_b64_tr_b16 v[244:245], v166 offset:52224
	ds_read_b64_tr_b16 v[248:249], v166 offset:52256
	ds_read_b64_tr_b16 v[198:199], v166 offset:52288
	ds_read_b64_tr_b16 v[202:203], v166 offset:52320
	ds_read_b64_tr_b16 v[246:247], v167 offset:52224
	ds_read_b64_tr_b16 v[250:251], v167 offset:52256
	ds_read_b64_tr_b16 v[200:201], v167 offset:52288
	ds_read_b64_tr_b16 v[204:205], v167 offset:52320
	ds_write_b64 v161, v[26:27] offset:26112
	v_mfma_f32_16x16x32_bf16 v[36:39], v[182:185], v[190:193], v[36:39]
	v_mfma_f32_16x16x32_bf16 v[32:35], v[186:189], v[190:193], v[32:35]
	s_waitcnt lgkmcnt(4)
	v_mfma_f32_16x16x32_bf16 v[156:159], v[244:247], v[194:197], v[156:159]
	ds_read_b128 v[182:185], v162 offset:37888
	s_waitcnt lgkmcnt(4)
	v_mfma_f32_16x16x32_bf16 v[152:155], v[248:251], v[194:197], v[152:155]
	s_waitcnt lgkmcnt(3)
	v_mfma_f32_16x16x32_bf16 v[148:151], v[198:201], v[194:197], v[148:151]
	s_waitcnt lgkmcnt(2)
	v_mfma_f32_16x16x32_bf16 v[144:147], v[202:205], v[194:197], v[144:147]
	v_mfma_f32_16x16x32_bf16 v[140:143], v[244:247], v[170:173], v[140:143]
	ds_read_b128 v[186:189], v162 offset:39936
	buffer_load_dwordx4 v[24:27], v160, s[12:15], s9 offen
	s_waitcnt vmcnt(11)
	v_cvt_pk_bf16_f32 v23, v22, v23
	v_cvt_pk_bf16_f32 v22, v20, v21
	v_mfma_f32_16x16x32_bf16 v[136:139], v[248:251], v[170:173], v[136:139]
	ds_write_b64 v161, v[22:23] offset:256
	v_mfma_f32_16x16x32_bf16 v[132:135], v[198:201], v[170:173], v[132:135]
	v_mfma_f32_16x16x32_bf16 v[128:131], v[202:205], v[170:173], v[128:131]
	s_waitcnt lgkmcnt(2)
	v_mfma_f32_16x16x32_bf16 v[124:127], v[244:247], v[182:185], v[124:127]
	ds_read_b128 v[170:173], v162 offset:41984
	v_mfma_f32_16x16x32_bf16 v[120:123], v[248:251], v[182:185], v[120:123]
	v_mfma_f32_16x16x32_bf16 v[116:119], v[198:201], v[182:185], v[116:119]
	v_mfma_f32_16x16x32_bf16 v[112:115], v[202:205], v[182:185], v[112:115]
	s_waitcnt lgkmcnt(2)
	v_mfma_f32_16x16x32_bf16 v[108:111], v[244:247], v[186:189], v[108:111]
	ds_read_b128 v[182:185], v162 offset:44032
	buffer_load_dwordx4 v[20:23], v160, s[16:19], s25 offen
	s_waitcnt vmcnt(11)
	v_cvt_pk_bf16_f32 v7, v6, v7
	v_cvt_pk_bf16_f32 v6, v4, v5
	v_mfma_f32_16x16x32_bf16 v[104:107], v[248:251], v[186:189], v[104:107]
	ds_write_b64 v161, v[6:7] offset:8960
	v_mfma_f32_16x16x32_bf16 v[100:103], v[198:201], v[186:189], v[100:103]
	v_mfma_f32_16x16x32_bf16 v[96:99], v[202:205], v[186:189], v[96:99]
	s_waitcnt lgkmcnt(2)
	v_mfma_f32_16x16x32_bf16 v[92:95], v[244:247], v[170:173], v[92:95]
	ds_read_b128 v[186:189], v162 offset:46080
	v_mfma_f32_16x16x32_bf16 v[88:91], v[248:251], v[170:173], v[88:91]
	v_mfma_f32_16x16x32_bf16 v[84:87], v[198:201], v[170:173], v[84:87]
	v_mfma_f32_16x16x32_bf16 v[80:83], v[202:205], v[170:173], v[80:83]
	s_waitcnt lgkmcnt(2)
	v_mfma_f32_16x16x32_bf16 v[76:79], v[244:247], v[182:185], v[76:79]
	ds_read_b128 v[252:255], v162 offset:48128
	buffer_load_dwordx4 v[4:7], v160, s[16:19], s26 offen
	s_waitcnt vmcnt(11)
	v_cvt_pk_bf16_f32 v11, v10, v11
	v_cvt_pk_bf16_f32 v10, v8, v9
	v_mfma_f32_16x16x32_bf16 v[72:75], v[248:251], v[182:185], v[72:75]
	ds_write_b64 v161, v[10:11] offset:17664
	v_mfma_f32_16x16x32_bf16 v[68:71], v[198:201], v[182:185], v[68:71]
	v_mfma_f32_16x16x32_bf16 v[64:67], v[202:205], v[182:185], v[64:67]
	s_waitcnt lgkmcnt(2)
	v_mfma_f32_16x16x32_bf16 v[60:63], v[244:247], v[186:189], v[60:63]
	v_mfma_f32_16x16x32_bf16 v[56:59], v[248:251], v[186:189], v[56:59]
	v_mfma_f32_16x16x32_bf16 v[52:55], v[198:201], v[186:189], v[52:55]
	v_mfma_f32_16x16x32_bf16 v[48:51], v[202:205], v[186:189], v[48:51]
	s_waitcnt lgkmcnt(1)
	buffer_load_dwordx4 v[8:11], v160, s[16:19], s27 offen
	s_waitcnt vmcnt(11)
	v_cvt_pk_bf16_f32 v19, v18, v19
	v_cvt_pk_bf16_f32 v18, v16, v17
	ds_write_b64 v161, v[18:19] offset:26368
	buffer_load_dwordx4 v[16:19], v160, s[16:19], s9 offen
	s_waitcnt vmcnt(8)
	s_waitcnt lgkmcnt(0)
	s_barrier
	s_add_i32 s8, s8, 2
	s_add_i32 s9, s9, 0x300000
	s_addk_i32 s24, 0x100
	s_cmp_ge_i32 s8, s64
	s_cbranch_scc0 .LBB0_71
	v_mfma_f32_16x16x32_bf16 v[44:47], v[244:247], v[252:255], v[44:47]
	v_mfma_f32_16x16x32_bf16 v[40:43], v[248:251], v[252:255], v[40:43]
	v_mfma_f32_16x16x32_bf16 v[36:39], v[198:201], v[252:255], v[36:39]
	v_mfma_f32_16x16x32_bf16 v[32:35], v[202:205], v[252:255], v[32:35]
	s_branch .LBB0_73

; #define G_ENDTILE(VM) do { asm volatile("s_waitcnt vmcnt(" #VM ")" ::: "memory"); \
;         asm volatile("s_waitcnt lgkmcnt(0)" ::: "memory"); __builtin_amdgcn_s_barrier(); asm volatile("" ::: "memory"); } while (0)
;     ...
;         for (int t = 0; t < nt - 2; t += 2) {
;             G_TILE(G_A0, G_B0, true, G_B1, G_A1, t + 1, true, t + 2, (void)0);
;             G_ENDTILE(8);
.LBB0_378:
	s_mov_b32 m0, s72
	s_add_i32 s25, s24, 0xffffff80
	ds_read_b64_tr_b16 v[170:171], v165
	ds_read_b64_tr_b16 v[172:173], v166
	ds_read_b64_tr_b16 v[176:177], v166 offset:32
	ds_read_b128 v[178:181], v162
	ds_read_b64_tr_b16 v[174:175], v165 offset:32
	ds_read_b64_tr_b16 v[182:183], v165 offset:64
	ds_read_b64_tr_b16 v[186:187], v165 offset:96
	ds_read_b64_tr_b16 v[184:185], v166 offset:64
	ds_read_b64_tr_b16 v[188:189], v166 offset:96
	ds_read_b128 v[190:193], v162 offset:2048
	ds_read_b128 v[198:201], v162 offset:4096
	buffer_load_dwordx4 v163, s[20:23], s25 offen lds
	s_mov_b32 m0, s71
	v_mfma_f32_16x16x32_bf16 v[44:47], v[244:247], v[252:255], v[44:47]
	v_mfma_f32_16x16x32_bf16 v[40:43], v[248:251], v[252:255], v[40:43]
	v_mfma_f32_16x16x32_bf16 v[36:39], v[202:205], v[252:255], v[36:39]
	v_mfma_f32_16x16x32_bf16 v[32:35], v[206:209], v[252:255], v[32:35]
	s_waitcnt lgkmcnt(7)
	v_mfma_f32_16x16x32_bf16 v[156:159], v[170:173], v[178:181], v[156:159]
	buffer_load_dwordx4 v164, s[20:23], s25 offen lds
	s_waitcnt lgkmcnt(6)
	v_mfma_f32_16x16x32_bf16 v[152:155], v[174:177], v[178:181], v[152:155]
	s_waitcnt lgkmcnt(3)
	v_mfma_f32_16x16x32_bf16 v[148:151], v[182:185], v[178:181], v[148:151]
	s_waitcnt lgkmcnt(2)
	v_mfma_f32_16x16x32_bf16 v[144:147], v[186:189], v[178:181], v[144:147]
	s_waitcnt lgkmcnt(1)
	v_mfma_f32_16x16x32_bf16 v[140:143], v[170:173], v[190:193], v[140:143]
	s_mov_b32 m0, s70
	s_nop 0
	buffer_load_dwordx4 v167, s[20:23], s25 offen lds
	ds_read_b128 v[178:181], v162 offset:6144
	s_waitcnt vmcnt(10)
	v_cvt_pk_bf16_f32 v15, v14, v15
	v_cvt_pk_bf16_f32 v14, v12, v13
	v_mfma_f32_16x16x32_bf16 v[136:139], v[174:177], v[190:193], v[136:139]
	ds_write_b64 v161, v[14:15] offset:34816
	v_mfma_f32_16x16x32_bf16 v[132:135], v[182:185], v[190:193], v[132:135]
	s_mov_b32 m0, s68
	s_nop 0
	buffer_load_dwordx4 v168, s[20:23], s25 offen lds
	s_add_i32 s25, s9, 0xfff20000
	v_mfma_f32_16x16x32_bf16 v[128:131], v[186:189], v[190:193], v[128:131]
	s_waitcnt lgkmcnt(2)
	v_mfma_f32_16x16x32_bf16 v[124:127], v[170:173], v[198:201], v[124:127]
	ds_read_b128 v[190:193], v162 offset:8192
	v_mfma_f32_16x16x32_bf16 v[120:123], v[174:177], v[198:201], v[120:123]
	v_mfma_f32_16x16x32_bf16 v[116:119], v[182:185], v[198:201], v[116:119]
	v_mfma_f32_16x16x32_bf16 v[112:115], v[186:189], v[198:201], v[112:115]
	s_waitcnt lgkmcnt(2)
	v_mfma_f32_16x16x32_bf16 v[108:111], v[170:173], v[178:181], v[108:111]
	ds_read_b128 v[198:201], v162 offset:10240
	buffer_load_dwordx4 v[12:15], v160, s[12:15], s25 offen
	s_waitcnt vmcnt(10)
	v_cvt_pk_bf16_f32 v31, v30, v31
	v_cvt_pk_bf16_f32 v30, v28, v29
	v_mfma_f32_16x16x32_bf16 v[104:107], v[174:177], v[178:181], v[104:107]
	ds_write_b64 v161, v[30:31] offset:43520
	v_mfma_f32_16x16x32_bf16 v[100:103], v[182:185], v[178:181], v[100:103]
	v_mfma_f32_16x16x32_bf16 v[96:99], v[186:189], v[178:181], v[96:99]
	s_add_i32 s26, s9, 0xfff40000
	s_waitcnt lgkmcnt(2)
	v_mfma_f32_16x16x32_bf16 v[92:95], v[170:173], v[190:193], v[92:95]
	ds_read_b128 v[178:181], v162 offset:12288
	v_mfma_f32_16x16x32_bf16 v[88:91], v[174:177], v[190:193], v[88:91]
	v_mfma_f32_16x16x32_bf16 v[84:87], v[182:185], v[190:193], v[84:87]
	v_mfma_f32_16x16x32_bf16 v[80:83], v[186:189], v[190:193], v[80:83]
	s_waitcnt lgkmcnt(2)
	v_mfma_f32_16x16x32_bf16 v[76:79], v[170:173], v[198:201], v[76:79]
	ds_read_b128 v[190:193], v162 offset:14336
	v_cvt_pk_bf16_f32 v7, v6, v7
	v_cvt_pk_bf16_f32 v6, v4, v5
	v_mfma_f32_16x16x32_bf16 v[72:75], v[174:177], v[198:201], v[72:75]
	ds_write_b64 v161, v[6:7] offset:52224
	v_mfma_f32_16x16x32_bf16 v[68:71], v[182:185], v[198:201], v[68:71]
	v_mfma_f32_16x16x32_bf16 v[64:67], v[186:189], v[198:201], v[64:67]
	s_add_i32 s27, s9, 0xfff60000
	buffer_load_dwordx4 v[28:31], v160, s[12:15], s26 offen
	s_waitcnt lgkmcnt(2)
	v_mfma_f32_16x16x32_bf16 v[60:63], v[170:173], v[178:181], v[60:63]
	ds_read_b128 v[198:201], v162 offset:1024
	v_mfma_f32_16x16x32_bf16 v[56:59], v[174:177], v[178:181], v[56:59]
	v_mfma_f32_16x16x32_bf16 v[52:55], v[182:185], v[178:181], v[52:55]
	v_mfma_f32_16x16x32_bf16 v[48:51], v[186:189], v[178:181], v[48:51]
	s_waitcnt lgkmcnt(2)
	v_mfma_f32_16x16x32_bf16 v[44:47], v[170:173], v[190:193], v[44:47]
	ds_read_b128 v[170:173], v162 offset:3072
	buffer_load_dwordx4 v[4:7], v160, s[12:15], s27 offen
	s_waitcnt vmcnt(11)
	v_cvt_pk_bf16_f32 v27, v26, v27
	v_cvt_pk_bf16_f32 v26, v24, v25
	v_mfma_f32_16x16x32_bf16 v[40:43], v[174:177], v[190:193], v[40:43]
	ds_read_b64_tr_b16 v[244:245], v165 offset:17408
	ds_read_b64_tr_b16 v[248:249], v165 offset:17440
	ds_read_b64_tr_b16 v[202:203], v165 offset:17472
	ds_read_b64_tr_b16 v[206:207], v165 offset:17504
	ds_read_b64_tr_b16 v[246:247], v166 offset:17408
	ds_read_b64_tr_b16 v[250:251], v166 offset:17440
	ds_read_b64_tr_b16 v[204:205], v166 offset:17472
	ds_read_b64_tr_b16 v[208:209], v166 offset:17504
	ds_write_b64 v161, v[26:27] offset:60928
	v_mfma_f32_16x16x32_bf16 v[36:39], v[182:185], v[190:193], v[36:39]
	v_mfma_f32_16x16x32_bf16 v[32:35], v[186:189], v[190:193], v[32:35]
	s_add_i32 s45, s9, 0xfff80000
	s_waitcnt lgkmcnt(4)
	v_mfma_f32_16x16x32_bf16 v[156:159], v[244:247], v[198:201], v[156:159]
	ds_read_b128 v[182:185], v162 offset:5120
	s_waitcnt lgkmcnt(4)
	v_mfma_f32_16x16x32_bf16 v[152:155], v[248:251], v[198:201], v[152:155]
	s_waitcnt lgkmcnt(3)
	v_mfma_f32_16x16x32_bf16 v[148:151], v[202:205], v[198:201], v[148:151]
	s_waitcnt lgkmcnt(2)
	v_mfma_f32_16x16x32_bf16 v[144:147], v[206:209], v[198:201], v[144:147]
	v_mfma_f32_16x16x32_bf16 v[140:143], v[244:247], v[170:173], v[140:143]
	ds_read_b128 v[186:189], v162 offset:7168
	buffer_load_dwordx4 v[24:27], v160, s[12:15], s45 offen
	s_waitcnt vmcnt(11)
; #define G_ENDTILE(VM) do { asm volatile("s_waitcnt vmcnt(" #VM ")" ::: "memory"); \
;         asm volatile("s_waitcnt lgkmcnt(0)" ::: "memory"); __builtin_amdgcn_s_barrier(); asm volatile("" ::: "memory"); } while (0)
;     ...
;         for (int t = 0; t < nt - 2; t += 2) {
;             G_TILE(G_A0, G_B0, true, G_B1, G_A1, t + 1, true, t + 2, (void)0);
;             G_ENDTILE(8);
;             G_TILE(G_A1, G_B1, true, G_B0, G_A0, t + 2, true, t + 3, (void)0);
;             G_ENDTILE(8);
	v_cvt_pk_bf16_f32 v23, v22, v23
	v_cvt_pk_bf16_f32 v22, v20, v21
	v_mfma_f32_16x16x32_bf16 v[136:139], v[248:251], v[170:173], v[136:139]
	ds_write_b64 v161, v[22:23] offset:35072
	v_mfma_f32_16x16x32_bf16 v[132:135], v[202:205], v[170:173], v[132:135]
	v_mfma_f32_16x16x32_bf16 v[128:131], v[206:209], v[170:173], v[128:131]
	s_waitcnt lgkmcnt(2)
	v_mfma_f32_16x16x32_bf16 v[124:127], v[244:247], v[182:185], v[124:127]
	ds_read_b128 v[170:173], v162 offset:9216
	v_mfma_f32_16x16x32_bf16 v[120:123], v[248:251], v[182:185], v[120:123]
	v_mfma_f32_16x16x32_bf16 v[116:119], v[202:205], v[182:185], v[116:119]
	v_mfma_f32_16x16x32_bf16 v[112:115], v[206:209], v[182:185], v[112:115]
	s_waitcnt lgkmcnt(2)
	v_mfma_f32_16x16x32_bf16 v[108:111], v[244:247], v[186:189], v[108:111]
	ds_read_b128 v[182:185], v162 offset:11264
	buffer_load_dwordx4 v[20:23], v160, s[16:19], s25 offen
	s_waitcnt vmcnt(10)
	v_cvt_pk_bf16_f32 v11, v10, v11
	v_cvt_pk_bf16_f32 v10, v8, v9
	v_mfma_f32_16x16x32_bf16 v[104:107], v[248:251], v[186:189], v[104:107]
	ds_write_b64 v161, v[10:11] offset:43776
	v_mfma_f32_16x16x32_bf16 v[100:103], v[202:205], v[186:189], v[100:103]
	v_mfma_f32_16x16x32_bf16 v[96:99], v[206:209], v[186:189], v[96:99]
	s_waitcnt lgkmcnt(2)
	v_mfma_f32_16x16x32_bf16 v[92:95], v[244:247], v[170:173], v[92:95]
	ds_read_b128 v[186:189], v162 offset:13312
	v_mfma_f32_16x16x32_bf16 v[88:91], v[248:251], v[170:173], v[88:91]
	v_mfma_f32_16x16x32_bf16 v[84:87], v[202:205], v[170:173], v[84:87]
	v_mfma_f32_16x16x32_bf16 v[80:83], v[206:209], v[170:173], v[80:83]
	s_waitcnt lgkmcnt(2)
	v_mfma_f32_16x16x32_bf16 v[76:79], v[244:247], v[182:185], v[76:79]
	ds_read_b128 v[252:255], v162 offset:15360
	v_cvt_pk_bf16_f32 v3, v2, v3
	v_cvt_pk_bf16_f32 v2, v0, v1
	v_mfma_f32_16x16x32_bf16 v[72:75], v[248:251], v[182:185], v[72:75]
	ds_write_b64 v161, v[2:3] offset:52480
	v_mfma_f32_16x16x32_bf16 v[68:71], v[202:205], v[182:185], v[68:71]
	v_mfma_f32_16x16x32_bf16 v[64:67], v[206:209], v[182:185], v[64:67]
	buffer_load_dwordx4 v[8:11], v160, s[16:19], s26 offen
	s_waitcnt lgkmcnt(2)
	v_mfma_f32_16x16x32_bf16 v[60:63], v[244:247], v[186:189], v[60:63]
	v_mfma_f32_16x16x32_bf16 v[56:59], v[248:251], v[186:189], v[56:59]
	v_mfma_f32_16x16x32_bf16 v[52:55], v[202:205], v[186:189], v[52:55]
	v_mfma_f32_16x16x32_bf16 v[48:51], v[206:209], v[186:189], v[48:51]
	s_waitcnt lgkmcnt(1)
	buffer_load_dwordx4 v[0:3], v160, s[16:19], s27 offen
	s_waitcnt vmcnt(11)
	v_cvt_pk_bf16_f32 v19, v18, v19
	v_cvt_pk_bf16_f32 v18, v16, v17
	ds_write_b64 v161, v[18:19] offset:61184
	buffer_load_dwordx4 v[16:19], v160, s[16:19], s45 offen
	s_waitcnt vmcnt(8)
	s_mov_b32 m0, s59
	s_waitcnt lgkmcnt(0)
	s_barrier
	ds_read_b64_tr_b16 v[170:171], v165 offset:34816
	ds_read_b64_tr_b16 v[172:173], v166 offset:34816
	ds_read_b64_tr_b16 v[176:177], v166 offset:34848
	ds_read_b128 v[178:181], v162 offset:32768
	ds_read_b64_tr_b16 v[174:175], v165 offset:34848
	ds_read_b64_tr_b16 v[182:183], v165 offset:34880
	ds_read_b64_tr_b16 v[186:187], v165 offset:34912
	ds_read_b64_tr_b16 v[184:185], v166 offset:34880
	ds_read_b64_tr_b16 v[188:189], v166 offset:34912
	ds_read_b128 v[190:193], v162 offset:34816
	ds_read_b128 v[198:201], v162 offset:36864
	buffer_load_dwordx4 v163, s[20:23], s24 offen lds
	s_mov_b32 m0, s60
	v_mfma_f32_16x16x32_bf16 v[44:47], v[244:247], v[252:255], v[44:47]
	v_mfma_f32_16x16x32_bf16 v[40:43], v[248:251], v[252:255], v[40:43]
	v_mfma_f32_16x16x32_bf16 v[36:39], v[202:205], v[252:255], v[36:39]
	v_mfma_f32_16x16x32_bf16 v[32:35], v[206:209], v[252:255], v[32:35]
	s_waitcnt lgkmcnt(7)
	v_mfma_f32_16x16x32_bf16 v[156:159], v[170:173], v[178:181], v[156:159]
	buffer_load_dwordx4 v164, s[20:23], s24 offen lds
	s_add_i32 s25, s9, 0xfffa0000
	s_waitcnt lgkmcnt(6)
	v_mfma_f32_16x16x32_bf16 v[152:155], v[174:177], v[178:181], v[152:155]
	s_waitcnt lgkmcnt(3)
	v_mfma_f32_16x16x32_bf16 v[148:151], v[182:185], v[178:181], v[148:151]
	s_waitcnt lgkmcnt(2)
	v_mfma_f32_16x16x32_bf16 v[144:147], v[186:189], v[178:181], v[144:147]
	s_waitcnt lgkmcnt(1)
	v_mfma_f32_16x16x32_bf16 v[140:143], v[170:173], v[190:193], v[140:143]
	s_mov_b32 m0, s61
	s_nop 0
	buffer_load_dwordx4 v167, s[20:23], s24 offen lds
	ds_read_b128 v[178:181], v162 offset:38912
	s_waitcnt vmcnt(10)
	v_cvt_pk_bf16_f32 v15, v14, v15
	v_cvt_pk_bf16_f32 v14, v12, v13
	v_mfma_f32_16x16x32_bf16 v[136:139], v[174:177], v[190:193], v[136:139]
	ds_write_b64 v161, v[14:15]
	v_mfma_f32_16x16x32_bf16 v[132:135], v[182:185], v[190:193], v[132:135]
	s_mov_b32 m0, s62
	s_nop 0
	buffer_load_dwordx4 v168, s[20:23], s24 offen lds
	v_mfma_f32_16x16x32_bf16 v[128:131], v[186:189], v[190:193], v[128:131]
	s_waitcnt lgkmcnt(2)
	v_mfma_f32_16x16x32_bf16 v[124:127], v[170:173], v[198:201], v[124:127]
	ds_read_b128 v[190:193], v162 offset:40960
	v_mfma_f32_16x16x32_bf16 v[120:123], v[174:177], v[198:201], v[120:123]
	v_mfma_f32_16x16x32_bf16 v[116:119], v[182:185], v[198:201], v[116:119]
	v_mfma_f32_16x16x32_bf16 v[112:115], v[186:189], v[198:201], v[112:115]
	s_waitcnt lgkmcnt(2)
	v_mfma_f32_16x16x32_bf16 v[108:111], v[170:173], v[178:181], v[108:111]
	ds_read_b128 v[198:201], v162 offset:43008
	buffer_load_dwordx4 v[12:15], v160, s[12:15], s25 offen
	s_waitcnt vmcnt(11)
	v_cvt_pk_bf16_f32 v31, v30, v31
	v_cvt_pk_bf16_f32 v30, v28, v29
	v_mfma_f32_16x16x32_bf16 v[104:107], v[174:177], v[178:181], v[104:107]
	ds_write_b64 v161, v[30:31] offset:8704
	v_mfma_f32_16x16x32_bf16 v[100:103], v[182:185], v[178:181], v[100:103]
	v_mfma_f32_16x16x32_bf16 v[96:99], v[186:189], v[178:181], v[96:99]
	s_add_i32 s26, s9, 0xfffc0000
	s_waitcnt lgkmcnt(2)
; #define G_ENDTILE(VM) do { asm volatile("s_waitcnt vmcnt(" #VM ")" ::: "memory"); \
;         asm volatile("s_waitcnt lgkmcnt(0)" ::: "memory"); __builtin_amdgcn_s_barrier(); asm volatile("" ::: "memory"); } while (0)
;     ...
;         for (int t = 0; t < nt - 2; t += 2) {
;             G_TILE(G_A0, G_B0, true, G_B1, G_A1, t + 1, true, t + 2, (void)0);
;             G_ENDTILE(8);
;             G_TILE(G_A1, G_B1, true, G_B0, G_A0, t + 2, true, t + 3, (void)0);
;             G_ENDTILE(8);
;         }
	v_mfma_f32_16x16x32_bf16 v[92:95], v[170:173], v[190:193], v[92:95]
	ds_read_b128 v[178:181], v162 offset:45056
	v_mfma_f32_16x16x32_bf16 v[88:91], v[174:177], v[190:193], v[88:91]
	v_mfma_f32_16x16x32_bf16 v[84:87], v[182:185], v[190:193], v[84:87]
	v_mfma_f32_16x16x32_bf16 v[80:83], v[186:189], v[190:193], v[80:83]
	s_waitcnt lgkmcnt(2)
	v_mfma_f32_16x16x32_bf16 v[76:79], v[170:173], v[198:201], v[76:79]
	ds_read_b128 v[190:193], v162 offset:47104
	buffer_load_dwordx4 v[28:31], v160, s[12:15], s26 offen
	s_waitcnt vmcnt(11)
	v_cvt_pk_bf16_f32 v7, v6, v7
	v_cvt_pk_bf16_f32 v6, v4, v5
	v_mfma_f32_16x16x32_bf16 v[72:75], v[174:177], v[198:201], v[72:75]
	ds_write_b64 v161, v[6:7] offset:17408
	v_mfma_f32_16x16x32_bf16 v[68:71], v[182:185], v[198:201], v[68:71]
	v_mfma_f32_16x16x32_bf16 v[64:67], v[186:189], v[198:201], v[64:67]
	s_add_i32 s27, s9, 0xfffe0000
	s_waitcnt lgkmcnt(2)
	v_mfma_f32_16x16x32_bf16 v[60:63], v[170:173], v[178:181], v[60:63]
	ds_read_b128 v[198:201], v162 offset:33792
	v_mfma_f32_16x16x32_bf16 v[56:59], v[174:177], v[178:181], v[56:59]
	v_mfma_f32_16x16x32_bf16 v[52:55], v[182:185], v[178:181], v[52:55]
	v_mfma_f32_16x16x32_bf16 v[48:51], v[186:189], v[178:181], v[48:51]
	s_waitcnt lgkmcnt(2)
	v_mfma_f32_16x16x32_bf16 v[44:47], v[170:173], v[190:193], v[44:47]
	ds_read_b128 v[170:173], v162 offset:35840
	buffer_load_dwordx4 v[4:7], v160, s[12:15], s27 offen
	s_waitcnt vmcnt(11)
	v_cvt_pk_bf16_f32 v27, v26, v27
	v_cvt_pk_bf16_f32 v26, v24, v25
	v_mfma_f32_16x16x32_bf16 v[40:43], v[174:177], v[190:193], v[40:43]
	ds_read_b64_tr_b16 v[244:245], v165 offset:52224
	ds_read_b64_tr_b16 v[248:249], v165 offset:52256
	ds_read_b64_tr_b16 v[202:203], v165 offset:52288
	ds_read_b64_tr_b16 v[206:207], v165 offset:52320
	ds_read_b64_tr_b16 v[246:247], v166 offset:52224
	ds_read_b64_tr_b16 v[250:251], v166 offset:52256
	ds_read_b64_tr_b16 v[204:205], v166 offset:52288
	ds_read_b64_tr_b16 v[208:209], v166 offset:52320
	ds_write_b64 v161, v[26:27] offset:26112
	v_mfma_f32_16x16x32_bf16 v[36:39], v[182:185], v[190:193], v[36:39]
	v_mfma_f32_16x16x32_bf16 v[32:35], v[186:189], v[190:193], v[32:35]
	s_waitcnt lgkmcnt(4)
	v_mfma_f32_16x16x32_bf16 v[156:159], v[244:247], v[198:201], v[156:159]
	ds_read_b128 v[182:185], v162 offset:37888
	s_waitcnt lgkmcnt(4)
	v_mfma_f32_16x16x32_bf16 v[152:155], v[248:251], v[198:201], v[152:155]
	s_waitcnt lgkmcnt(3)
	v_mfma_f32_16x16x32_bf16 v[148:151], v[202:205], v[198:201], v[148:151]
	s_waitcnt lgkmcnt(2)
	v_mfma_f32_16x16x32_bf16 v[144:147], v[206:209], v[198:201], v[144:147]
	v_mfma_f32_16x16x32_bf16 v[140:143], v[244:247], v[170:173], v[140:143]
	ds_read_b128 v[186:189], v162 offset:39936
	buffer_load_dwordx4 v[24:27], v160, s[12:15], s9 offen
	s_waitcnt vmcnt(11)
	v_cvt_pk_bf16_f32 v23, v22, v23
	v_cvt_pk_bf16_f32 v22, v20, v21
	v_mfma_f32_16x16x32_bf16 v[136:139], v[248:251], v[170:173], v[136:139]
	ds_write_b64 v161, v[22:23] offset:256
	v_mfma_f32_16x16x32_bf16 v[132:135], v[202:205], v[170:173], v[132:135]
	v_mfma_f32_16x16x32_bf16 v[128:131], v[206:209], v[170:173], v[128:131]
	s_waitcnt lgkmcnt(2)
	v_mfma_f32_16x16x32_bf16 v[124:127], v[244:247], v[182:185], v[124:127]
	ds_read_b128 v[170:173], v162 offset:41984
	v_mfma_f32_16x16x32_bf16 v[120:123], v[248:251], v[182:185], v[120:123]
	v_mfma_f32_16x16x32_bf16 v[116:119], v[202:205], v[182:185], v[116:119]
	v_mfma_f32_16x16x32_bf16 v[112:115], v[206:209], v[182:185], v[112:115]
	s_waitcnt lgkmcnt(2)
	v_mfma_f32_16x16x32_bf16 v[108:111], v[244:247], v[186:189], v[108:111]
	ds_read_b128 v[182:185], v162 offset:44032
	buffer_load_dwordx4 v[20:23], v160, s[16:19], s25 offen
	s_waitcnt vmcnt(11)
	v_cvt_pk_bf16_f32 v11, v10, v11
	v_cvt_pk_bf16_f32 v10, v8, v9
	v_mfma_f32_16x16x32_bf16 v[104:107], v[248:251], v[186:189], v[104:107]
	ds_write_b64 v161, v[10:11] offset:8960
	v_mfma_f32_16x16x32_bf16 v[100:103], v[202:205], v[186:189], v[100:103]
	v_mfma_f32_16x16x32_bf16 v[96:99], v[206:209], v[186:189], v[96:99]
	s_waitcnt lgkmcnt(2)
	v_mfma_f32_16x16x32_bf16 v[92:95], v[244:247], v[170:173], v[92:95]
	ds_read_b128 v[186:189], v162 offset:46080
	v_mfma_f32_16x16x32_bf16 v[88:91], v[248:251], v[170:173], v[88:91]
	v_mfma_f32_16x16x32_bf16 v[84:87], v[202:205], v[170:173], v[84:87]
	v_mfma_f32_16x16x32_bf16 v[80:83], v[206:209], v[170:173], v[80:83]
	s_waitcnt lgkmcnt(2)
	v_mfma_f32_16x16x32_bf16 v[76:79], v[244:247], v[182:185], v[76:79]
	ds_read_b128 v[252:255], v162 offset:48128
	buffer_load_dwordx4 v[8:11], v160, s[16:19], s26 offen
	s_waitcnt vmcnt(11)
	v_cvt_pk_bf16_f32 v3, v2, v3
	v_cvt_pk_bf16_f32 v2, v0, v1
	v_mfma_f32_16x16x32_bf16 v[72:75], v[248:251], v[182:185], v[72:75]
	ds_write_b64 v161, v[2:3] offset:17664
	v_mfma_f32_16x16x32_bf16 v[68:71], v[202:205], v[182:185], v[68:71]
	v_mfma_f32_16x16x32_bf16 v[64:67], v[206:209], v[182:185], v[64:67]
	s_waitcnt lgkmcnt(2)
	v_mfma_f32_16x16x32_bf16 v[60:63], v[244:247], v[186:189], v[60:63]
	v_mfma_f32_16x16x32_bf16 v[56:59], v[248:251], v[186:189], v[56:59]
	v_mfma_f32_16x16x32_bf16 v[52:55], v[202:205], v[186:189], v[52:55]
	v_mfma_f32_16x16x32_bf16 v[48:51], v[206:209], v[186:189], v[48:51]
	s_waitcnt lgkmcnt(1)
	buffer_load_dwordx4 v[0:3], v160, s[16:19], s27 offen
	s_waitcnt vmcnt(11)
	v_cvt_pk_bf16_f32 v19, v18, v19
	v_cvt_pk_bf16_f32 v18, v16, v17
	ds_write_b64 v161, v[18:19] offset:26368
	buffer_load_dwordx4 v[16:19], v160, s[16:19], s9 offen
	s_waitcnt vmcnt(8)
	s_waitcnt lgkmcnt(0)
	s_barrier
	s_add_i32 s8, s8, 2
	s_add_i32 s9, s9, 0x100000
	s_addk_i32 s24, 0x100
	s_cmp_ge_i32 s8, s67
	s_cbranch_scc0 .LBB0_378
	v_mfma_f32_16x16x32_bf16 v[44:47], v[244:247], v[252:255], v[44:47]
	v_mfma_f32_16x16x32_bf16 v[40:43], v[248:251], v[252:255], v[40:43]
	v_mfma_f32_16x16x32_bf16 v[36:39], v[202:205], v[252:255], v[36:39]
	v_mfma_f32_16x16x32_bf16 v[32:35], v[206:209], v[252:255], v[32:35]
	s_branch .LBB0_380

; #define G_ENDTILE(VM) do { asm volatile("s_waitcnt vmcnt(" #VM ")" ::: "memory"); \
;         asm volatile("s_waitcnt lgkmcnt(0)" ::: "memory"); __builtin_amdgcn_s_barrier(); asm volatile("" ::: "memory"); } while (0)
;     ...
;         for (int t = 0; t < nt - 2; t += 2) {
;             G_TILE(G_A0, G_B0, true, G_B1, G_A1, t + 1, true, t + 2, (void)0);
;             G_ENDTILE(8);
.LBB0_651:
	s_mov_b32 m0, s85
	s_add_i32 s37, s36, 0xffffff80
	ds_read_b64_tr_b16 v[178:179], v188
	ds_read_b64_tr_b16 v[176:177], v187
	ds_read_b64_tr_b16 v[180:181], v187 offset:32
	ds_read_b64_tr_b16 v[198:199], v187 offset:64
	ds_read_b64_tr_b16 v[202:203], v187 offset:96
	ds_read_b128 v[206:209], v186
	ds_read_b64_tr_b16 v[182:183], v188 offset:32
	ds_read_b64_tr_b16 v[200:201], v188 offset:64
	ds_read_b64_tr_b16 v[204:205], v188 offset:96
	ds_read_b128 v[210:213], v186 offset:2048
	ds_read_b128 v[214:217], v186 offset:4096
	buffer_load_dwordx4 v189, s[20:23], s37 offen lds
	s_mov_b32 m0, s7
	v_mfma_f32_16x16x32_bf16 v[44:47], v[244:247], v[238:241], v[44:47]
	v_mfma_f32_16x16x32_bf16 v[40:43], v[218:221], v[238:241], v[40:43]
	v_mfma_f32_16x16x32_bf16 v[36:39], v[248:251], v[238:241], v[36:39]
	v_mfma_f32_16x16x32_bf16 v[32:35], v[252:255], v[238:241], v[32:35]
	s_waitcnt lgkmcnt(5)
	v_mfma_f32_16x16x32_bf16 v[172:175], v[176:179], v[206:209], v[172:175]
	buffer_load_dwordx4 v192, s[20:23], s37 offen lds
	s_waitcnt lgkmcnt(4)
	v_mfma_f32_16x16x32_bf16 v[168:171], v[180:183], v[206:209], v[168:171]
	s_waitcnt lgkmcnt(3)
	v_mfma_f32_16x16x32_bf16 v[164:167], v[198:201], v[206:209], v[164:167]
	s_waitcnt lgkmcnt(2)
	v_mfma_f32_16x16x32_bf16 v[160:163], v[202:205], v[206:209], v[160:163]
	s_waitcnt lgkmcnt(1)
	v_mfma_f32_16x16x32_bf16 v[156:159], v[176:179], v[210:213], v[156:159]
	s_mov_b32 m0, s6
	s_nop 0
	buffer_load_dwordx4 v191, s[20:23], s37 offen lds
	ds_read_b128 v[206:209], v186 offset:6144
	s_waitcnt vmcnt(10)
	v_cvt_pk_bf16_f32 v15, v14, v15
	v_cvt_pk_bf16_f32 v14, v12, v13
	v_mfma_f32_16x16x32_bf16 v[152:155], v[180:183], v[210:213], v[152:155]
	ds_write_b64 v185, v[14:15] offset:34816
	v_mfma_f32_16x16x32_bf16 v[148:151], v[198:201], v[210:213], v[148:151]
	s_mov_b32 m0, s47
	s_nop 0
	buffer_load_dwordx4 v190, s[20:23], s37 offen lds
	v_mfma_f32_16x16x32_bf16 v[144:147], v[202:205], v[210:213], v[144:147]
	s_waitcnt lgkmcnt(2)
	v_mfma_f32_16x16x32_bf16 v[132:135], v[176:179], v[214:217], v[132:135]
	s_mov_b32 m0, s48
	s_nop 0
	buffer_load_dwordx4 v193, s[20:23], s37 offen lds
	s_add_i32 s37, s17, 0xfff20000
	ds_read_b128 v[210:213], v186 offset:8192
	v_mfma_f32_16x16x32_bf16 v[124:127], v[180:183], v[214:217], v[124:127]
	v_mfma_f32_16x16x32_bf16 v[120:123], v[198:201], v[214:217], v[120:123]
	v_mfma_f32_16x16x32_bf16 v[140:143], v[202:205], v[214:217], v[140:143]
	s_waitcnt lgkmcnt(2)
	v_mfma_f32_16x16x32_bf16 v[136:139], v[176:179], v[206:209], v[136:139]
	ds_read_b128 v[214:217], v186 offset:10240
	buffer_load_dwordx4 v[12:15], v184, s[24:27], s37 offen
	s_waitcnt vmcnt(12)
	v_cvt_pk_bf16_f32 v3, v2, v3
	v_cvt_pk_bf16_f32 v2, v0, v1
	v_mfma_f32_16x16x32_bf16 v[128:131], v[180:183], v[206:209], v[128:131]
	ds_write_b64 v185, v[2:3] offset:43520
	v_mfma_f32_16x16x32_bf16 v[116:119], v[198:201], v[206:209], v[116:119]
	v_mfma_f32_16x16x32_bf16 v[112:115], v[202:205], v[206:209], v[112:115]
	s_add_i32 s38, s17, 0xfff40000
	s_waitcnt lgkmcnt(2)
	v_mfma_f32_16x16x32_bf16 v[100:103], v[176:179], v[210:213], v[100:103]
	ds_read_b128 v[206:209], v186 offset:12288
	v_mfma_f32_16x16x32_bf16 v[92:95], v[180:183], v[210:213], v[92:95]
	v_mfma_f32_16x16x32_bf16 v[88:91], v[198:201], v[210:213], v[88:91]
	v_mfma_f32_16x16x32_bf16 v[108:111], v[202:205], v[210:213], v[108:111]
	s_waitcnt lgkmcnt(2)
	v_mfma_f32_16x16x32_bf16 v[104:107], v[176:179], v[214:217], v[104:107]
	ds_read_b128 v[210:213], v186 offset:14336
	buffer_load_dwordx4 v[0:3], v184, s[24:27], s38 offen
	s_waitcnt vmcnt(12)
	v_cvt_pk_bf16_f32 v31, v30, v31
	v_cvt_pk_bf16_f32 v30, v28, v29
	v_mfma_f32_16x16x32_bf16 v[96:99], v[180:183], v[214:217], v[96:99]
	ds_write_b64 v185, v[30:31] offset:52224
	v_mfma_f32_16x16x32_bf16 v[84:87], v[198:201], v[214:217], v[84:87]
	v_mfma_f32_16x16x32_bf16 v[80:83], v[202:205], v[214:217], v[80:83]
	s_add_i32 s39, s17, 0xfff60000
	s_waitcnt lgkmcnt(2)
	v_mfma_f32_16x16x32_bf16 v[72:75], v[176:179], v[206:209], v[72:75]
	ds_read_b128 v[214:217], v186 offset:16384
	v_mfma_f32_16x16x32_bf16 v[64:67], v[180:183], v[206:209], v[64:67]
	v_mfma_f32_16x16x32_bf16 v[60:63], v[198:201], v[206:209], v[60:63]
	v_mfma_f32_16x16x32_bf16 v[76:79], v[202:205], v[206:209], v[76:79]
	s_waitcnt lgkmcnt(2)
	v_mfma_f32_16x16x32_bf16 v[68:71], v[176:179], v[210:213], v[68:71]
	ds_read_b128 v[206:209], v186 offset:1024
	buffer_load_dwordx4 v[28:31], v184, s[24:27], s39 offen
	s_waitcnt vmcnt(12)
	v_cvt_pk_bf16_f32 v27, v26, v27
	v_cvt_pk_bf16_f32 v26, v24, v25
	v_mfma_f32_16x16x32_bf16 v[56:59], v[180:183], v[210:213], v[56:59]
	ds_write_b64 v185, v[26:27] offset:60928
	v_mfma_f32_16x16x32_bf16 v[52:55], v[198:201], v[210:213], v[52:55]
	v_mfma_f32_16x16x32_bf16 v[48:51], v[202:205], v[210:213], v[48:51]
	s_add_i32 s42, s17, 0xfff80000
	ds_read_b128 v[210:213], v186 offset:3072
	s_waitcnt lgkmcnt(3)
	v_mfma_f32_16x16x32_bf16 v[44:47], v[176:179], v[214:217], v[44:47]
	ds_read_b64_tr_b16 v[246:247], v188 offset:17408
	ds_read_b64_tr_b16 v[220:221], v188 offset:17440
	ds_read_b64_tr_b16 v[244:245], v187 offset:17408
	ds_read_b64_tr_b16 v[218:219], v187 offset:17440
	v_mfma_f32_16x16x32_bf16 v[40:43], v[180:183], v[214:217], v[40:43]
	ds_read_b64_tr_b16 v[248:249], v187 offset:17472
	ds_read_b64_tr_b16 v[250:251], v188 offset:17472
	v_mfma_f32_16x16x32_bf16 v[36:39], v[198:201], v[214:217], v[36:39]
	ds_read_b64_tr_b16 v[252:253], v187 offset:17504
	ds_read_b64_tr_b16 v[254:255], v188 offset:17504
	v_mfma_f32_16x16x32_bf16 v[32:35], v[202:205], v[214:217], v[32:35]
	s_waitcnt lgkmcnt(5)
; #define G_ENDTILE(VM) do { asm volatile("s_waitcnt vmcnt(" #VM ")" ::: "memory"); \
;         asm volatile("s_waitcnt lgkmcnt(0)" ::: "memory"); __builtin_amdgcn_s_barrier(); asm volatile("" ::: "memory"); } while (0)
;     ...
;         for (int t = 0; t < nt - 2; t += 2) {
;             G_TILE(G_A0, G_B0, true, G_B1, G_A1, t + 1, true, t + 2, (void)0);
;             G_ENDTILE(8);
;             G_TILE(G_A1, G_B1, true, G_B0, G_A0, t + 2, true, t + 3, (void)0);
;             G_ENDTILE(8);
	v_mfma_f32_16x16x32_bf16 v[172:175], v[244:247], v[206:209], v[172:175]
	ds_read_b128 v[202:205], v186 offset:5120
	buffer_load_dwordx4 v[24:27], v184, s[24:27], s42 offen
	s_waitcnt vmcnt(12)
	v_cvt_pk_bf16_f32 v23, v22, v23
	v_cvt_pk_bf16_f32 v22, v20, v21
	s_waitcnt lgkmcnt(5)
	v_mfma_f32_16x16x32_bf16 v[168:171], v[218:221], v[206:209], v[168:171]
	ds_write_b64 v185, v[22:23] offset:34880
	s_waitcnt lgkmcnt(4)
	v_mfma_f32_16x16x32_bf16 v[164:167], v[248:251], v[206:209], v[164:167]
	s_waitcnt lgkmcnt(2)
	v_mfma_f32_16x16x32_bf16 v[160:163], v[252:255], v[206:209], v[160:163]
	v_mfma_f32_16x16x32_bf16 v[156:159], v[244:247], v[210:213], v[156:159]
	ds_read_b128 v[206:209], v186 offset:7168
	v_mfma_f32_16x16x32_bf16 v[152:155], v[218:221], v[210:213], v[152:155]
	v_mfma_f32_16x16x32_bf16 v[148:151], v[248:251], v[210:213], v[148:151]
	v_mfma_f32_16x16x32_bf16 v[144:147], v[252:255], v[210:213], v[144:147]
	s_waitcnt lgkmcnt(2)
	v_mfma_f32_16x16x32_bf16 v[132:135], v[244:247], v[202:205], v[132:135]
	ds_read_b128 v[210:213], v186 offset:9216
	buffer_load_dwordx4 v[20:23], v184, s[28:31], s37 offen
	s_waitcnt vmcnt(12)
	v_cvt_pk_bf16_f32 v7, v6, v7
	v_cvt_pk_bf16_f32 v6, v4, v5
	v_mfma_f32_16x16x32_bf16 v[124:127], v[218:221], v[202:205], v[124:127]
	ds_write_b64 v185, v[6:7] offset:43584
	v_mfma_f32_16x16x32_bf16 v[120:123], v[248:251], v[202:205], v[120:123]
	v_mfma_f32_16x16x32_bf16 v[140:143], v[252:255], v[202:205], v[140:143]
	s_waitcnt lgkmcnt(2)
	v_mfma_f32_16x16x32_bf16 v[136:139], v[244:247], v[206:209], v[136:139]
	ds_read_b128 v[202:205], v186 offset:11264
	v_mfma_f32_16x16x32_bf16 v[128:131], v[218:221], v[206:209], v[128:131]
	v_mfma_f32_16x16x32_bf16 v[116:119], v[248:251], v[206:209], v[116:119]
	v_mfma_f32_16x16x32_bf16 v[112:115], v[252:255], v[206:209], v[112:115]
	s_waitcnt lgkmcnt(2)
	v_mfma_f32_16x16x32_bf16 v[100:103], v[244:247], v[210:213], v[100:103]
	ds_read_b128 v[206:209], v186 offset:13312
	buffer_load_dwordx4 v[4:7], v184, s[28:31], s38 offen
	s_waitcnt vmcnt(12)
	v_cvt_pk_bf16_f32 v11, v10, v11
	v_cvt_pk_bf16_f32 v10, v8, v9
	v_mfma_f32_16x16x32_bf16 v[92:95], v[218:221], v[210:213], v[92:95]
	ds_write_b64 v185, v[10:11] offset:52288
	v_mfma_f32_16x16x32_bf16 v[88:91], v[248:251], v[210:213], v[88:91]
	v_mfma_f32_16x16x32_bf16 v[108:111], v[252:255], v[210:213], v[108:111]
	s_waitcnt lgkmcnt(2)
	v_mfma_f32_16x16x32_bf16 v[104:107], v[244:247], v[202:205], v[104:107]
	ds_read_b128 v[210:213], v186 offset:15360
	v_mfma_f32_16x16x32_bf16 v[96:99], v[218:221], v[202:205], v[96:99]
	v_mfma_f32_16x16x32_bf16 v[84:87], v[248:251], v[202:205], v[84:87]
	v_mfma_f32_16x16x32_bf16 v[80:83], v[252:255], v[202:205], v[80:83]
	s_waitcnt lgkmcnt(2)
	v_mfma_f32_16x16x32_bf16 v[72:75], v[244:247], v[206:209], v[72:75]
	ds_read_b128 v[238:241], v186 offset:17408
	buffer_load_dwordx4 v[8:11], v184, s[28:31], s39 offen
	s_waitcnt vmcnt(12)
	v_cvt_pk_bf16_f32 v19, v18, v19
	v_cvt_pk_bf16_f32 v18, v16, v17
	v_mfma_f32_16x16x32_bf16 v[64:67], v[218:221], v[206:209], v[64:67]
	ds_write_b64 v185, v[18:19] offset:60992
	v_mfma_f32_16x16x32_bf16 v[60:63], v[248:251], v[206:209], v[60:63]
	v_mfma_f32_16x16x32_bf16 v[76:79], v[252:255], v[206:209], v[76:79]
	s_waitcnt lgkmcnt(2)
	v_mfma_f32_16x16x32_bf16 v[68:71], v[244:247], v[210:213], v[68:71]
	v_mfma_f32_16x16x32_bf16 v[56:59], v[218:221], v[210:213], v[56:59]
	v_mfma_f32_16x16x32_bf16 v[52:55], v[248:251], v[210:213], v[52:55]
	v_mfma_f32_16x16x32_bf16 v[48:51], v[252:255], v[210:213], v[48:51]
	s_waitcnt lgkmcnt(1)
	buffer_load_dwordx4 v[16:19], v184, s[28:31], s42 offen
	s_waitcnt vmcnt(8)
	s_mov_b32 m0, s46
	s_waitcnt lgkmcnt(0)
	s_barrier
	ds_read_b64_tr_b16 v[178:179], v188 offset:34816
	ds_read_b64_tr_b16 v[176:177], v187 offset:34816
	ds_read_b64_tr_b16 v[180:181], v187 offset:34848
	ds_read_b64_tr_b16 v[198:199], v187 offset:34880
	ds_read_b64_tr_b16 v[202:203], v187 offset:34912
	ds_read_b128 v[206:209], v186 offset:36864
	ds_read_b64_tr_b16 v[182:183], v188 offset:34848
	ds_read_b64_tr_b16 v[200:201], v188 offset:34880
	ds_read_b64_tr_b16 v[204:205], v188 offset:34912
	ds_read_b128 v[210:213], v186 offset:38912
	ds_read_b128 v[214:217], v186 offset:40960
	buffer_load_dwordx4 v189, s[20:23], s36 offen lds
	s_mov_b32 m0, s86
	v_mfma_f32_16x16x32_bf16 v[44:47], v[244:247], v[238:241], v[44:47]
	v_mfma_f32_16x16x32_bf16 v[40:43], v[218:221], v[238:241], v[40:43]
	v_mfma_f32_16x16x32_bf16 v[36:39], v[248:251], v[238:241], v[36:39]
	v_mfma_f32_16x16x32_bf16 v[32:35], v[252:255], v[238:241], v[32:35]
	s_waitcnt lgkmcnt(5)
	v_mfma_f32_16x16x32_bf16 v[172:175], v[176:179], v[206:209], v[172:175]
	buffer_load_dwordx4 v192, s[20:23], s36 offen lds
	s_add_i32 s37, s17, 0xfffa0000
	s_waitcnt lgkmcnt(4)
	v_mfma_f32_16x16x32_bf16 v[168:171], v[180:183], v[206:209], v[168:171]
	s_waitcnt lgkmcnt(3)
	v_mfma_f32_16x16x32_bf16 v[164:167], v[198:201], v[206:209], v[164:167]
	s_waitcnt lgkmcnt(2)
	v_mfma_f32_16x16x32_bf16 v[160:163], v[202:205], v[206:209], v[160:163]
	s_waitcnt lgkmcnt(1)
	v_mfma_f32_16x16x32_bf16 v[156:159], v[176:179], v[210:213], v[156:159]
	s_mov_b32 m0, s89
	s_nop 0
	buffer_load_dwordx4 v191, s[20:23], s36 offen lds
	ds_read_b128 v[206:209], v186 offset:43008
	s_waitcnt vmcnt(10)
	v_cvt_pk_bf16_f32 v15, v14, v15
	v_cvt_pk_bf16_f32 v14, v12, v13
	v_mfma_f32_16x16x32_bf16 v[152:155], v[180:183], v[210:213], v[152:155]
	ds_write_b64 v185, v[14:15]
	v_mfma_f32_16x16x32_bf16 v[148:151], v[198:201], v[210:213], v[148:151]
	s_mov_b32 m0, s90
	s_nop 0
	buffer_load_dwordx4 v190, s[20:23], s36 offen lds
	v_mfma_f32_16x16x32_bf16 v[144:147], v[202:205], v[210:213], v[144:147]
	s_waitcnt lgkmcnt(2)
	v_mfma_f32_16x16x32_bf16 v[132:135], v[176:179], v[214:217], v[132:135]
	s_mov_b32 m0, s91
	s_nop 0
	buffer_load_dwordx4 v193, s[20:23], s36 offen lds
	ds_read_b128 v[210:213], v186 offset:45056
	v_mfma_f32_16x16x32_bf16 v[124:127], v[180:183], v[214:217], v[124:127]
	v_mfma_f32_16x16x32_bf16 v[120:123], v[198:201], v[214:217], v[120:123]
	v_mfma_f32_16x16x32_bf16 v[140:143], v[202:205], v[214:217], v[140:143]
	s_waitcnt lgkmcnt(2)
	v_mfma_f32_16x16x32_bf16 v[136:139], v[176:179], v[206:209], v[136:139]
	ds_read_b128 v[214:217], v186 offset:47104
	buffer_load_dwordx4 v[12:15], v184, s[24:27], s37 offen
	s_waitcnt vmcnt(12)
	v_cvt_pk_bf16_f32 v3, v2, v3
	v_cvt_pk_bf16_f32 v2, v0, v1
	v_mfma_f32_16x16x32_bf16 v[128:131], v[180:183], v[206:209], v[128:131]
	ds_write_b64 v185, v[2:3] offset:8704
	v_mfma_f32_16x16x32_bf16 v[116:119], v[198:201], v[206:209], v[116:119]
	v_mfma_f32_16x16x32_bf16 v[112:115], v[202:205], v[206:209], v[112:115]
	s_add_i32 s38, s17, 0xfffc0000
	s_waitcnt lgkmcnt(2)
	v_mfma_f32_16x16x32_bf16 v[100:103], v[176:179], v[210:213], v[100:103]
	ds_read_b128 v[206:209], v186 offset:49152
	v_mfma_f32_16x16x32_bf16 v[92:95], v[180:183], v[210:213], v[92:95]
	v_mfma_f32_16x16x32_bf16 v[88:91], v[198:201], v[210:213], v[88:91]
	v_mfma_f32_16x16x32_bf16 v[108:111], v[202:205], v[210:213], v[108:111]
	s_waitcnt lgkmcnt(2)
	v_mfma_f32_16x16x32_bf16 v[104:107], v[176:179], v[214:217], v[104:107]
	ds_read_b128 v[210:213], v186 offset:51200
	buffer_load_dwordx4 v[0:3], v184, s[24:27], s38 offen
	s_waitcnt vmcnt(12)
	v_cvt_pk_bf16_f32 v31, v30, v31
	v_cvt_pk_bf16_f32 v30, v28, v29
	v_mfma_f32_16x16x32_bf16 v[96:99], v[180:183], v[214:217], v[96:99]
	ds_write_b64 v185, v[30:31] offset:17408
	v_mfma_f32_16x16x32_bf16 v[84:87], v[198:201], v[214:217], v[84:87]
	v_mfma_f32_16x16x32_bf16 v[80:83], v[202:205], v[214:217], v[80:83]
	s_add_i32 s39, s17, 0xfffe0000
	s_waitcnt lgkmcnt(2)
	v_mfma_f32_16x16x32_bf16 v[72:75], v[176:179], v[206:209], v[72:75]
	ds_read_b128 v[214:217], v186 offset:53248
	v_mfma_f32_16x16x32_bf16 v[64:67], v[180:183], v[206:209], v[64:67]
	v_mfma_f32_16x16x32_bf16 v[60:63], v[198:201], v[206:209], v[60:63]
	v_mfma_f32_16x16x32_bf16 v[76:79], v[202:205], v[206:209], v[76:79]
	s_waitcnt lgkmcnt(2)
	v_mfma_f32_16x16x32_bf16 v[68:71], v[176:179], v[210:213], v[68:71]
	ds_read_b128 v[206:209], v186 offset:37888
	buffer_load_dwordx4 v[28:31], v184, s[24:27], s39 offen
	s_waitcnt vmcnt(12)
	v_cvt_pk_bf16_f32 v27, v26, v27
	v_cvt_pk_bf16_f32 v26, v24, v25
	v_mfma_f32_16x16x32_bf16 v[56:59], v[180:183], v[210:213], v[56:59]
	ds_write_b64 v185, v[26:27] offset:26112
	v_mfma_f32_16x16x32_bf16 v[52:55], v[198:201], v[210:213], v[52:55]
	v_mfma_f32_16x16x32_bf16 v[48:51], v[202:205], v[210:213], v[48:51]
	ds_read_b128 v[210:213], v186 offset:39936
	s_waitcnt lgkmcnt(3)
	v_mfma_f32_16x16x32_bf16 v[44:47], v[176:179], v[214:217], v[44:47]
	ds_read_b64_tr_b16 v[246:247], v188 offset:52224
	ds_read_b64_tr_b16 v[220:221], v188 offset:52256
	ds_read_b64_tr_b16 v[244:245], v187 offset:52224
	ds_read_b64_tr_b16 v[218:219], v187 offset:52256
	v_mfma_f32_16x16x32_bf16 v[40:43], v[180:183], v[214:217], v[40:43]
	ds_read_b64_tr_b16 v[248:249], v187 offset:52288
	ds_read_b64_tr_b16 v[250:251], v188 offset:52288
	v_mfma_f32_16x16x32_bf16 v[36:39], v[198:201], v[214:217], v[36:39]
	ds_read_b64_tr_b16 v[252:253], v187 offset:52320
	ds_read_b64_tr_b16 v[254:255], v188 offset:52320
	v_mfma_f32_16x16x32_bf16 v[32:35], v[202:205], v[214:217], v[32:35]
	s_waitcnt lgkmcnt(5)
	v_mfma_f32_16x16x32_bf16 v[172:175], v[244:247], v[206:209], v[172:175]
	ds_read_b128 v[202:205], v186 offset:41984
	buffer_load_dwordx4 v[24:27], v184, s[24:27], s17 offen
	s_waitcnt vmcnt(12)
	v_cvt_pk_bf16_f32 v23, v22, v23
	v_cvt_pk_bf16_f32 v22, v20, v21
	s_waitcnt lgkmcnt(5)
; #define G_ENDTILE(VM) do { asm volatile("s_waitcnt vmcnt(" #VM ")" ::: "memory"); \
;         asm volatile("s_waitcnt lgkmcnt(0)" ::: "memory"); __builtin_amdgcn_s_barrier(); asm volatile("" ::: "memory"); } while (0)
;     ...
;         for (int t = 0; t < nt - 2; t += 2) {
;             G_TILE(G_A0, G_B0, true, G_B1, G_A1, t + 1, true, t + 2, (void)0);
;             G_ENDTILE(8);
;             G_TILE(G_A1, G_B1, true, G_B0, G_A0, t + 2, true, t + 3, (void)0);
;             G_ENDTILE(8);
;         }
	v_mfma_f32_16x16x32_bf16 v[168:171], v[218:221], v[206:209], v[168:171]
	ds_write_b64 v185, v[22:23] offset:64
	s_waitcnt lgkmcnt(4)
	v_mfma_f32_16x16x32_bf16 v[164:167], v[248:251], v[206:209], v[164:167]
	s_waitcnt lgkmcnt(2)
	v_mfma_f32_16x16x32_bf16 v[160:163], v[252:255], v[206:209], v[160:163]
	v_mfma_f32_16x16x32_bf16 v[156:159], v[244:247], v[210:213], v[156:159]
	ds_read_b128 v[206:209], v186 offset:44032
	v_mfma_f32_16x16x32_bf16 v[152:155], v[218:221], v[210:213], v[152:155]
	v_mfma_f32_16x16x32_bf16 v[148:151], v[248:251], v[210:213], v[148:151]
	v_mfma_f32_16x16x32_bf16 v[144:147], v[252:255], v[210:213], v[144:147]
	s_waitcnt lgkmcnt(2)
	v_mfma_f32_16x16x32_bf16 v[132:135], v[244:247], v[202:205], v[132:135]
	ds_read_b128 v[210:213], v186 offset:46080
	buffer_load_dwordx4 v[20:23], v184, s[28:31], s37 offen
	s_waitcnt vmcnt(12)
	v_cvt_pk_bf16_f32 v7, v6, v7
	v_cvt_pk_bf16_f32 v6, v4, v5
	v_mfma_f32_16x16x32_bf16 v[124:127], v[218:221], v[202:205], v[124:127]
	ds_write_b64 v185, v[6:7] offset:8768
	v_mfma_f32_16x16x32_bf16 v[120:123], v[248:251], v[202:205], v[120:123]
	v_mfma_f32_16x16x32_bf16 v[140:143], v[252:255], v[202:205], v[140:143]
	s_waitcnt lgkmcnt(2)
	v_mfma_f32_16x16x32_bf16 v[136:139], v[244:247], v[206:209], v[136:139]
	ds_read_b128 v[202:205], v186 offset:48128
	v_mfma_f32_16x16x32_bf16 v[128:131], v[218:221], v[206:209], v[128:131]
	v_mfma_f32_16x16x32_bf16 v[116:119], v[248:251], v[206:209], v[116:119]
	v_mfma_f32_16x16x32_bf16 v[112:115], v[252:255], v[206:209], v[112:115]
	s_waitcnt lgkmcnt(2)
	v_mfma_f32_16x16x32_bf16 v[100:103], v[244:247], v[210:213], v[100:103]
	ds_read_b128 v[206:209], v186 offset:50176
	buffer_load_dwordx4 v[4:7], v184, s[28:31], s38 offen
	s_waitcnt vmcnt(12)
	v_cvt_pk_bf16_f32 v11, v10, v11
	v_cvt_pk_bf16_f32 v10, v8, v9
	v_mfma_f32_16x16x32_bf16 v[92:95], v[218:221], v[210:213], v[92:95]
	ds_write_b64 v185, v[10:11] offset:17472
	v_mfma_f32_16x16x32_bf16 v[88:91], v[248:251], v[210:213], v[88:91]
	v_mfma_f32_16x16x32_bf16 v[108:111], v[252:255], v[210:213], v[108:111]
	s_waitcnt lgkmcnt(2)
	v_mfma_f32_16x16x32_bf16 v[104:107], v[244:247], v[202:205], v[104:107]
	ds_read_b128 v[210:213], v186 offset:52224
	v_mfma_f32_16x16x32_bf16 v[96:99], v[218:221], v[202:205], v[96:99]
	v_mfma_f32_16x16x32_bf16 v[84:87], v[248:251], v[202:205], v[84:87]
	v_mfma_f32_16x16x32_bf16 v[80:83], v[252:255], v[202:205], v[80:83]
	s_waitcnt lgkmcnt(2)
	v_mfma_f32_16x16x32_bf16 v[72:75], v[244:247], v[206:209], v[72:75]
	ds_read_b128 v[238:241], v186 offset:54272
	buffer_load_dwordx4 v[8:11], v184, s[28:31], s39 offen
	s_waitcnt vmcnt(12)
	v_cvt_pk_bf16_f32 v19, v18, v19
	v_cvt_pk_bf16_f32 v18, v16, v17
	v_mfma_f32_16x16x32_bf16 v[64:67], v[218:221], v[206:209], v[64:67]
	ds_write_b64 v185, v[18:19] offset:26176
	v_mfma_f32_16x16x32_bf16 v[60:63], v[248:251], v[206:209], v[60:63]
	v_mfma_f32_16x16x32_bf16 v[76:79], v[252:255], v[206:209], v[76:79]
	s_waitcnt lgkmcnt(2)
	v_mfma_f32_16x16x32_bf16 v[68:71], v[244:247], v[210:213], v[68:71]
	v_mfma_f32_16x16x32_bf16 v[56:59], v[218:221], v[210:213], v[56:59]
	v_mfma_f32_16x16x32_bf16 v[52:55], v[248:251], v[210:213], v[52:55]
	v_mfma_f32_16x16x32_bf16 v[48:51], v[252:255], v[210:213], v[48:51]
	s_waitcnt lgkmcnt(1)
	buffer_load_dwordx4 v[16:19], v184, s[28:31], s17 offen
	s_waitcnt vmcnt(8)
	s_waitcnt lgkmcnt(0)
	s_barrier
	s_add_i32 s16, s16, 2
	s_add_i32 s17, s17, 0x100000
	s_addk_i32 s36, 0x100
	s_cmp_ge_i32 s16, s97
	s_cbranch_scc0 .LBB0_651
	v_mfma_f32_16x16x32_bf16 v[44:47], v[244:247], v[238:241], v[44:47]
	v_mfma_f32_16x16x32_bf16 v[40:43], v[218:221], v[238:241], v[40:43]
	v_mfma_f32_16x16x32_bf16 v[36:39], v[248:251], v[238:241], v[36:39]
	v_mfma_f32_16x16x32_bf16 v[32:35], v[252:255], v[238:241], v[32:35]
	s_branch .LBB0_653

.Lchk5_s2:
	buffer_load_dwordx4 v192, s[20:23], s37 offen lds
	s_waitcnt lgkmcnt(1)
	s_waitcnt vmcnt(9)
	s_cmp_le_u32 s99, 1
	s_cbranch_scc1 .Lchk5_s3
	v_mfma_f32_16x16x32_bf16 v[156:159], v[176:179], v[210:213], v[156:159]
	v_mfma_f32_16x16x32_bf16 v[152:155], v[180:183], v[210:213], v[152:155]
	v_mfma_f32_16x16x32_bf16 v[148:151], v[198:201], v[210:213], v[148:151]
	v_mfma_f32_16x16x32_bf16 v[144:147], v[202:205], v[210:213], v[144:147]
.Lchk5_s3:
	s_mov_b32 m0, s6
	s_nop 0
	buffer_load_dwordx4 v191, s[20:23], s37 offen lds
	ds_read_b128 v[206:209], v186 offset:6144
	v_cvt_pk_bf16_f32 v15, v14, v15
	v_cvt_pk_bf16_f32 v14, v12, v13
	ds_write_b64 v185, v[14:15] offset:34816
	s_mov_b32 m0, s47
	s_nop 0
	buffer_load_dwordx4 v190, s[20:23], s37 offen lds
	s_waitcnt lgkmcnt(2)
	s_cmp_le_u32 s99, 2
	s_cbranch_scc1 .Lchk5_s4
	v_mfma_f32_16x16x32_bf16 v[132:135], v[176:179], v[214:217], v[132:135]
	v_mfma_f32_16x16x32_bf16 v[124:127], v[180:183], v[214:217], v[124:127]
	v_mfma_f32_16x16x32_bf16 v[120:123], v[198:201], v[214:217], v[120:123]
	v_mfma_f32_16x16x32_bf16 v[140:143], v[202:205], v[214:217], v[140:143]
.Lchk5_s4:
	s_mov_b32 m0, s48
	s_nop 0
	buffer_load_dwordx4 v193, s[20:23], s37 offen lds
	s_add_i32 s37, s17, 0xfff20000
	ds_read_b128 v[210:213], v186 offset:8192
	s_waitcnt lgkmcnt(2)
	s_waitcnt vmcnt(11)
	s_cmp_le_u32 s99, 3
	s_cbranch_scc1 .Lchk5_s5
	v_mfma_f32_16x16x32_bf16 v[136:139], v[176:179], v[206:209], v[136:139]
	v_mfma_f32_16x16x32_bf16 v[128:131], v[180:183], v[206:209], v[128:131]
	v_mfma_f32_16x16x32_bf16 v[116:119], v[198:201], v[206:209], v[116:119]
	v_mfma_f32_16x16x32_bf16 v[112:115], v[202:205], v[206:209], v[112:115]

.Lchk5_s20:
	buffer_load_dwordx4 v192, s[20:23], s36 offen lds
	s_add_i32 s37, s17, 0xfffa0000
	s_waitcnt lgkmcnt(1)
	s_waitcnt vmcnt(9)
	s_cmp_le_u32 s99, 1
	s_cbranch_scc1 .Lchk5_s21
	v_mfma_f32_16x16x32_bf16 v[156:159], v[176:179], v[210:213], v[156:159]
	v_mfma_f32_16x16x32_bf16 v[152:155], v[180:183], v[210:213], v[152:155]
	v_mfma_f32_16x16x32_bf16 v[148:151], v[198:201], v[210:213], v[148:151]
	v_mfma_f32_16x16x32_bf16 v[144:147], v[202:205], v[210:213], v[144:147]
.Lchk5_s21:
	s_mov_b32 m0, s89
	s_nop 0
	buffer_load_dwordx4 v191, s[20:23], s36 offen lds
	ds_read_b128 v[206:209], v186 offset:43008
	v_cvt_pk_bf16_f32 v15, v14, v15
	v_cvt_pk_bf16_f32 v14, v12, v13
	ds_write_b64 v185, v[14:15]
	s_mov_b32 m0, s90
	s_nop 0
	buffer_load_dwordx4 v190, s[20:23], s36 offen lds
	s_waitcnt lgkmcnt(2)
	s_cmp_le_u32 s99, 2
	s_cbranch_scc1 .Lchk5_s22
	v_mfma_f32_16x16x32_bf16 v[132:135], v[176:179], v[214:217], v[132:135]
	v_mfma_f32_16x16x32_bf16 v[124:127], v[180:183], v[214:217], v[124:127]
	v_mfma_f32_16x16x32_bf16 v[120:123], v[198:201], v[214:217], v[120:123]
	v_mfma_f32_16x16x32_bf16 v[140:143], v[202:205], v[214:217], v[140:143]
.Lchk5_s22:
	s_mov_b32 m0, s91
	s_nop 0
	buffer_load_dwordx4 v193, s[20:23], s36 offen lds
	ds_read_b128 v[210:213], v186 offset:45056
	s_waitcnt lgkmcnt(2)
	s_waitcnt vmcnt(11)
	s_cmp_le_u32 s99, 3
	s_cbranch_scc1 .Lchk5_s23
	v_mfma_f32_16x16x32_bf16 v[136:139], v[176:179], v[206:209], v[136:139]
	v_mfma_f32_16x16x32_bf16 v[128:131], v[180:183], v[206:209], v[128:131]
	v_mfma_f32_16x16x32_bf16 v[116:119], v[198:201], v[206:209], v[116:119]
	v_mfma_f32_16x16x32_bf16 v[112:115], v[202:205], v[206:209], v[112:115]

; #define G_ENDTILE(VM) do { asm volatile("s_waitcnt vmcnt(" #VM ")" ::: "memory"); \
;         asm volatile("s_waitcnt lgkmcnt(0)" ::: "memory"); __builtin_amdgcn_s_barrier(); asm volatile("" ::: "memory"); } while (0)
;     ...
;         for (int t = 0; t < nt - 2; t += 2) {
;             G_TILE(G_A0, G_B0, true, G_B1, G_A1, t + 1, true, t + 2, (void)0);
;             G_ENDTILE(8);
.LBB0_863:
	s_mov_b32 m0, s85
	s_add_i32 s38, s36, 0xffffff80
	ds_read_b64_tr_b16 v[178:179], v206
	ds_read_b64_tr_b16 v[176:177], v205
	ds_read_b64_tr_b16 v[180:181], v205 offset:32
	ds_read_b64_tr_b16 v[184:185], v205 offset:64
	ds_read_b64_tr_b16 v[188:189], v205 offset:96
	ds_read_b128 v[192:195], v199
	ds_read_b64_tr_b16 v[182:183], v206 offset:32
	ds_read_b64_tr_b16 v[186:187], v206 offset:64
	ds_read_b64_tr_b16 v[190:191], v206 offset:96
	ds_read_b128 v[208:211], v199 offset:2048
	ds_read_b128 v[212:215], v199 offset:4096
	buffer_load_dwordx4 v200, s[20:23], s38 offen lds
	s_mov_b32 m0, s86
	v_mfma_f32_16x16x32_bf16 v[44:47], v[244:247], v[252:255], v[44:47]
	v_mfma_f32_16x16x32_bf16 v[40:43], v[248:251], v[252:255], v[40:43]
	v_mfma_f32_16x16x32_bf16 v[36:39], v[216:219], v[252:255], v[36:39]
	v_mfma_f32_16x16x32_bf16 v[32:35], v[220:223], v[252:255], v[32:35]
	s_waitcnt lgkmcnt(0)
	v_mfma_f32_16x16x32_bf16 v[172:175], v[176:179], v[192:195], v[172:175]
	buffer_load_dwordx4 v201, s[20:23], s38 offen lds
	v_mfma_f32_16x16x32_bf16 v[168:171], v[180:183], v[192:195], v[168:171]
	v_mfma_f32_16x16x32_bf16 v[164:167], v[184:187], v[192:195], v[164:167]
	v_mfma_f32_16x16x32_bf16 v[160:163], v[188:191], v[192:195], v[160:163]
	v_mfma_f32_16x16x32_bf16 v[156:159], v[176:179], v[208:211], v[156:159]
	s_mov_b32 m0, s87
	s_nop 0
	buffer_load_dwordx4 v202, s[20:23], s38 offen lds
	ds_read_b128 v[192:195], v199 offset:6144
	s_waitcnt vmcnt(10)
	v_cvt_pk_bf16_f32 v23, v22, v23
	v_cvt_pk_bf16_f32 v22, v20, v21
	v_mfma_f32_16x16x32_bf16 v[152:155], v[180:183], v[208:211], v[152:155]
	ds_write_b64 v198, v[22:23] offset:34816
	v_mfma_f32_16x16x32_bf16 v[148:151], v[184:187], v[208:211], v[148:151]
	s_mov_b32 m0, s88
	s_nop 0
	buffer_load_dwordx4 v203, s[20:23], s38 offen lds
	v_mfma_f32_16x16x32_bf16 v[144:147], v[188:191], v[208:211], v[144:147]
	v_mfma_f32_16x16x32_bf16 v[132:135], v[176:179], v[212:215], v[132:135]
	s_mov_b32 m0, s89
	s_nop 0
	buffer_load_dwordx4 v204, s[20:23], s38 offen lds
	s_add_i32 s38, s9, 0xfff20000
	ds_read_b128 v[208:211], v199 offset:8192
	v_mfma_f32_16x16x32_bf16 v[124:127], v[180:183], v[212:215], v[124:127]
	v_mfma_f32_16x16x32_bf16 v[120:123], v[184:187], v[212:215], v[120:123]
	v_mfma_f32_16x16x32_bf16 v[140:143], v[188:191], v[212:215], v[140:143]
	s_waitcnt lgkmcnt(2)
	v_mfma_f32_16x16x32_bf16 v[136:139], v[176:179], v[192:195], v[136:139]
	ds_read_b128 v[212:215], v199 offset:10240
	buffer_load_dwordx4 v[20:23], v197, s[24:27], s38 offen
	s_waitcnt vmcnt(11)
	v_cvt_pk_bf16_f32 v31, v30, v31
	v_cvt_pk_bf16_f32 v30, v28, v29
	v_mfma_f32_16x16x32_bf16 v[128:131], v[180:183], v[192:195], v[128:131]
	ds_write_b64 v198, v[30:31] offset:43520
	v_mfma_f32_16x16x32_bf16 v[116:119], v[184:187], v[192:195], v[116:119]
	v_mfma_f32_16x16x32_bf16 v[112:115], v[188:191], v[192:195], v[112:115]
	s_add_i32 s39, s9, 0xfff40000
	s_waitcnt lgkmcnt(2)
	v_mfma_f32_16x16x32_bf16 v[100:103], v[176:179], v[208:211], v[100:103]
	ds_read_b128 v[192:195], v199 offset:12288
	v_mfma_f32_16x16x32_bf16 v[92:95], v[180:183], v[208:211], v[92:95]
	v_mfma_f32_16x16x32_bf16 v[88:91], v[184:187], v[208:211], v[88:91]
	v_mfma_f32_16x16x32_bf16 v[108:111], v[188:191], v[208:211], v[108:111]
	s_waitcnt lgkmcnt(2)
	v_mfma_f32_16x16x32_bf16 v[104:107], v[176:179], v[212:215], v[104:107]
	ds_read_b128 v[208:211], v199 offset:14336
	v_cvt_pk_bf16_f32 v19, v18, v19
	v_cvt_pk_bf16_f32 v18, v16, v17
	v_mfma_f32_16x16x32_bf16 v[96:99], v[180:183], v[212:215], v[96:99]
	ds_write_b64 v198, v[18:19] offset:52224
	v_mfma_f32_16x16x32_bf16 v[84:87], v[184:187], v[212:215], v[84:87]
	v_mfma_f32_16x16x32_bf16 v[80:83], v[188:191], v[212:215], v[80:83]
	s_add_i32 s43, s9, 0xfff60000
	buffer_load_dwordx4 v[28:31], v197, s[24:27], s39 offen
	s_waitcnt lgkmcnt(2)
	v_mfma_f32_16x16x32_bf16 v[72:75], v[176:179], v[192:195], v[72:75]
	ds_read_b128 v[212:215], v199 offset:16384
	v_mfma_f32_16x16x32_bf16 v[64:67], v[180:183], v[192:195], v[64:67]
	v_mfma_f32_16x16x32_bf16 v[60:63], v[184:187], v[192:195], v[60:63]
	v_mfma_f32_16x16x32_bf16 v[76:79], v[188:191], v[192:195], v[76:79]
	s_waitcnt lgkmcnt(2)
	v_mfma_f32_16x16x32_bf16 v[68:71], v[176:179], v[208:211], v[68:71]
	ds_read_b128 v[192:195], v199 offset:1024
	buffer_load_dwordx4 v[16:19], v197, s[24:27], s43 offen
	s_waitcnt vmcnt(12)
	v_cvt_pk_bf16_f32 v27, v26, v27
	v_cvt_pk_bf16_f32 v26, v24, v25
	v_mfma_f32_16x16x32_bf16 v[56:59], v[180:183], v[208:211], v[56:59]
	ds_write_b64 v198, v[26:27] offset:60928
	v_mfma_f32_16x16x32_bf16 v[52:55], v[184:187], v[208:211], v[52:55]
	v_mfma_f32_16x16x32_bf16 v[48:51], v[188:191], v[208:211], v[48:51]
	s_add_i32 s45, s9, 0xfff80000
	ds_read_b128 v[208:211], v199 offset:3072
	s_waitcnt lgkmcnt(3)
	v_mfma_f32_16x16x32_bf16 v[44:47], v[176:179], v[212:215], v[44:47]
	ds_read_b64_tr_b16 v[246:247], v206 offset:17408
	ds_read_b64_tr_b16 v[218:219], v206 offset:17440
	ds_read_b64_tr_b16 v[244:245], v205 offset:17408
	ds_read_b64_tr_b16 v[216:217], v205 offset:17440
	v_mfma_f32_16x16x32_bf16 v[40:43], v[180:183], v[212:215], v[40:43]
	ds_read_b64_tr_b16 v[248:249], v205 offset:17472
	ds_read_b64_tr_b16 v[250:251], v206 offset:17472
	v_mfma_f32_16x16x32_bf16 v[36:39], v[184:187], v[212:215], v[36:39]
	ds_read_b64_tr_b16 v[252:253], v205 offset:17504
	ds_read_b64_tr_b16 v[254:255], v206 offset:17504
	v_mfma_f32_16x16x32_bf16 v[32:35], v[188:191], v[212:215], v[32:35]
	s_waitcnt lgkmcnt(5)
	v_mfma_f32_16x16x32_bf16 v[172:175], v[244:247], v[192:195], v[172:175]
	ds_read_b128 v[188:191], v199 offset:5120
	buffer_load_dwordx4 v[24:27], v197, s[24:27], s45 offen
	s_waitcnt vmcnt(12)
; #define G_ENDTILE(VM) do { asm volatile("s_waitcnt vmcnt(" #VM ")" ::: "memory"); \
;         asm volatile("s_waitcnt lgkmcnt(0)" ::: "memory"); __builtin_amdgcn_s_barrier(); asm volatile("" ::: "memory"); } while (0)
;     ...
;         for (int t = 0; t < nt - 2; t += 2) {
;             G_TILE(G_A0, G_B0, true, G_B1, G_A1, t + 1, true, t + 2, (void)0);
;             G_ENDTILE(8);
;             G_TILE(G_A1, G_B1, true, G_B0, G_A0, t + 2, true, t + 3, (void)0);
;             G_ENDTILE(8);
	v_cvt_pk_bf16_f32 v15, v14, v15
	v_cvt_pk_bf16_f32 v14, v12, v13
	s_waitcnt lgkmcnt(5)
	v_mfma_f32_16x16x32_bf16 v[168:171], v[216:219], v[192:195], v[168:171]
	ds_write_b64 v198, v[14:15] offset:35072
	s_waitcnt lgkmcnt(4)
	v_mfma_f32_16x16x32_bf16 v[164:167], v[248:251], v[192:195], v[164:167]
	s_waitcnt lgkmcnt(2)
	v_mfma_f32_16x16x32_bf16 v[160:163], v[252:255], v[192:195], v[160:163]
	v_mfma_f32_16x16x32_bf16 v[156:159], v[244:247], v[208:211], v[156:159]
	ds_read_b128 v[192:195], v199 offset:7168
	v_mfma_f32_16x16x32_bf16 v[152:155], v[216:219], v[208:211], v[152:155]
	v_mfma_f32_16x16x32_bf16 v[148:151], v[248:251], v[208:211], v[148:151]
	v_mfma_f32_16x16x32_bf16 v[144:147], v[252:255], v[208:211], v[144:147]
	s_waitcnt lgkmcnt(2)
	v_mfma_f32_16x16x32_bf16 v[132:135], v[244:247], v[188:191], v[132:135]
	ds_read_b128 v[208:211], v199 offset:9216
	buffer_load_dwordx4 v[12:15], v197, s[16:19], s38 offen
	s_waitcnt vmcnt(11)
	v_cvt_pk_bf16_f32 v7, v6, v7
	v_cvt_pk_bf16_f32 v6, v4, v5
	v_mfma_f32_16x16x32_bf16 v[124:127], v[216:219], v[188:191], v[124:127]
	ds_write_b64 v198, v[6:7] offset:43776
	v_mfma_f32_16x16x32_bf16 v[120:123], v[248:251], v[188:191], v[120:123]
	v_mfma_f32_16x16x32_bf16 v[140:143], v[252:255], v[188:191], v[140:143]
	s_waitcnt lgkmcnt(2)
	v_mfma_f32_16x16x32_bf16 v[136:139], v[244:247], v[192:195], v[136:139]
	ds_read_b128 v[188:191], v199 offset:11264
	v_mfma_f32_16x16x32_bf16 v[128:131], v[216:219], v[192:195], v[128:131]
	v_mfma_f32_16x16x32_bf16 v[116:119], v[248:251], v[192:195], v[116:119]
	v_mfma_f32_16x16x32_bf16 v[112:115], v[252:255], v[192:195], v[112:115]
	s_waitcnt lgkmcnt(2)
	v_mfma_f32_16x16x32_bf16 v[100:103], v[244:247], v[208:211], v[100:103]
	ds_read_b128 v[192:195], v199 offset:13312
	v_cvt_pk_bf16_f32 v3, v2, v3
	v_cvt_pk_bf16_f32 v2, v0, v1
	v_mfma_f32_16x16x32_bf16 v[92:95], v[216:219], v[208:211], v[92:95]
	ds_write_b64 v198, v[2:3] offset:52480
	v_mfma_f32_16x16x32_bf16 v[88:91], v[248:251], v[208:211], v[88:91]
	v_mfma_f32_16x16x32_bf16 v[108:111], v[252:255], v[208:211], v[108:111]
	buffer_load_dwordx4 v[4:7], v197, s[16:19], s39 offen
	s_waitcnt lgkmcnt(2)
	v_mfma_f32_16x16x32_bf16 v[104:107], v[244:247], v[188:191], v[104:107]
	ds_read_b128 v[208:211], v199 offset:15360
	v_mfma_f32_16x16x32_bf16 v[96:99], v[216:219], v[188:191], v[96:99]
	v_mfma_f32_16x16x32_bf16 v[84:87], v[248:251], v[188:191], v[84:87]
	v_mfma_f32_16x16x32_bf16 v[80:83], v[252:255], v[188:191], v[80:83]
	s_waitcnt lgkmcnt(2)
	v_mfma_f32_16x16x32_bf16 v[72:75], v[244:247], v[192:195], v[72:75]
	ds_read_b128 v[236:239], v199 offset:17408
	buffer_load_dwordx4 v[0:3], v197, s[16:19], s43 offen
	s_waitcnt vmcnt(12)
	v_cvt_pk_bf16_f32 v11, v10, v11
	v_cvt_pk_bf16_f32 v10, v8, v9
	v_mfma_f32_16x16x32_bf16 v[64:67], v[216:219], v[192:195], v[64:67]
	ds_write_b64 v198, v[10:11] offset:61184
	v_mfma_f32_16x16x32_bf16 v[60:63], v[248:251], v[192:195], v[60:63]
	v_mfma_f32_16x16x32_bf16 v[76:79], v[252:255], v[192:195], v[76:79]
	s_waitcnt lgkmcnt(2)
	v_mfma_f32_16x16x32_bf16 v[68:71], v[244:247], v[208:211], v[68:71]
	v_mfma_f32_16x16x32_bf16 v[56:59], v[216:219], v[208:211], v[56:59]
	v_mfma_f32_16x16x32_bf16 v[52:55], v[248:251], v[208:211], v[52:55]
	v_mfma_f32_16x16x32_bf16 v[48:51], v[252:255], v[208:211], v[48:51]
	s_waitcnt lgkmcnt(1)
	buffer_load_dwordx4 v[8:11], v197, s[16:19], s45 offen
	s_waitcnt vmcnt(8)
	s_mov_b32 m0, s49
	s_waitcnt lgkmcnt(0)
	s_barrier
	ds_read_b64_tr_b16 v[178:179], v206 offset:34816
	ds_read_b64_tr_b16 v[176:177], v205 offset:34816
	ds_read_b64_tr_b16 v[180:181], v205 offset:34848
	ds_read_b64_tr_b16 v[184:185], v205 offset:34880
	ds_read_b64_tr_b16 v[188:189], v205 offset:34912
	ds_read_b128 v[192:195], v199 offset:36864
	ds_read_b64_tr_b16 v[182:183], v206 offset:34848
	ds_read_b64_tr_b16 v[186:187], v206 offset:34880
	ds_read_b64_tr_b16 v[190:191], v206 offset:34912
	ds_read_b128 v[208:211], v199 offset:38912
	ds_read_b128 v[212:215], v199 offset:40960
	buffer_load_dwordx4 v200, s[20:23], s36 offen lds
	s_mov_b32 m0, s68
	v_mfma_f32_16x16x32_bf16 v[44:47], v[244:247], v[236:239], v[44:47]
	v_mfma_f32_16x16x32_bf16 v[40:43], v[216:219], v[236:239], v[40:43]
	v_mfma_f32_16x16x32_bf16 v[36:39], v[248:251], v[236:239], v[36:39]
	v_mfma_f32_16x16x32_bf16 v[32:35], v[252:255], v[236:239], v[32:35]
	s_waitcnt lgkmcnt(5)
	v_mfma_f32_16x16x32_bf16 v[172:175], v[176:179], v[192:195], v[172:175]
	buffer_load_dwordx4 v201, s[20:23], s36 offen lds
	s_add_i32 s38, s9, 0xfffa0000
	s_waitcnt lgkmcnt(4)
	v_mfma_f32_16x16x32_bf16 v[168:171], v[180:183], v[192:195], v[168:171]
	s_waitcnt lgkmcnt(3)
	v_mfma_f32_16x16x32_bf16 v[164:167], v[184:187], v[192:195], v[164:167]
	s_waitcnt lgkmcnt(2)
	v_mfma_f32_16x16x32_bf16 v[160:163], v[188:191], v[192:195], v[160:163]
	s_waitcnt lgkmcnt(1)
	v_mfma_f32_16x16x32_bf16 v[156:159], v[176:179], v[208:211], v[156:159]
	s_mov_b32 m0, s77
	s_nop 0
	buffer_load_dwordx4 v202, s[20:23], s36 offen lds
	ds_read_b128 v[192:195], v199 offset:43008
	s_waitcnt vmcnt(10)
	v_cvt_pk_bf16_f32 v23, v22, v23
	v_cvt_pk_bf16_f32 v22, v20, v21
	v_mfma_f32_16x16x32_bf16 v[152:155], v[180:183], v[208:211], v[152:155]
	ds_write_b64 v198, v[22:23]
	v_mfma_f32_16x16x32_bf16 v[148:151], v[184:187], v[208:211], v[148:151]
	s_mov_b32 m0, s78
	s_nop 0
	buffer_load_dwordx4 v203, s[20:23], s36 offen lds
	v_mfma_f32_16x16x32_bf16 v[144:147], v[188:191], v[208:211], v[144:147]
	s_waitcnt lgkmcnt(2)
	v_mfma_f32_16x16x32_bf16 v[132:135], v[176:179], v[212:215], v[132:135]
	s_mov_b32 m0, s79
	s_nop 0
	buffer_load_dwordx4 v204, s[20:23], s36 offen lds
	ds_read_b128 v[208:211], v199 offset:45056
	v_mfma_f32_16x16x32_bf16 v[124:127], v[180:183], v[212:215], v[124:127]
	v_mfma_f32_16x16x32_bf16 v[120:123], v[184:187], v[212:215], v[120:123]
	v_mfma_f32_16x16x32_bf16 v[140:143], v[188:191], v[212:215], v[140:143]
	s_waitcnt lgkmcnt(2)
	v_mfma_f32_16x16x32_bf16 v[136:139], v[176:179], v[192:195], v[136:139]
	ds_read_b128 v[212:215], v199 offset:47104
	buffer_load_dwordx4 v[20:23], v197, s[24:27], s38 offen
	s_waitcnt vmcnt(12)
	v_cvt_pk_bf16_f32 v31, v30, v31
	v_cvt_pk_bf16_f32 v30, v28, v29
	v_mfma_f32_16x16x32_bf16 v[128:131], v[180:183], v[192:195], v[128:131]
	ds_write_b64 v198, v[30:31] offset:8704
	v_mfma_f32_16x16x32_bf16 v[116:119], v[184:187], v[192:195], v[116:119]
	v_mfma_f32_16x16x32_bf16 v[112:115], v[188:191], v[192:195], v[112:115]
	s_add_i32 s39, s9, 0xfffc0000
	s_waitcnt lgkmcnt(2)
	v_mfma_f32_16x16x32_bf16 v[100:103], v[176:179], v[208:211], v[100:103]
	ds_read_b128 v[192:195], v199 offset:49152
	v_mfma_f32_16x16x32_bf16 v[92:95], v[180:183], v[208:211], v[92:95]
	v_mfma_f32_16x16x32_bf16 v[88:91], v[184:187], v[208:211], v[88:91]
	v_mfma_f32_16x16x32_bf16 v[108:111], v[188:191], v[208:211], v[108:111]
	s_waitcnt lgkmcnt(2)
	v_mfma_f32_16x16x32_bf16 v[104:107], v[176:179], v[212:215], v[104:107]
	ds_read_b128 v[208:211], v199 offset:51200
	buffer_load_dwordx4 v[28:31], v197, s[24:27], s39 offen
	s_waitcnt vmcnt(12)
	v_cvt_pk_bf16_f32 v19, v18, v19
	v_cvt_pk_bf16_f32 v18, v16, v17
	v_mfma_f32_16x16x32_bf16 v[96:99], v[180:183], v[212:215], v[96:99]
	ds_write_b64 v198, v[18:19] offset:17408
	v_mfma_f32_16x16x32_bf16 v[84:87], v[184:187], v[212:215], v[84:87]
	v_mfma_f32_16x16x32_bf16 v[80:83], v[188:191], v[212:215], v[80:83]
	s_add_i32 s43, s9, 0xfffe0000
	s_waitcnt lgkmcnt(2)
	v_mfma_f32_16x16x32_bf16 v[72:75], v[176:179], v[192:195], v[72:75]
	ds_read_b128 v[212:215], v199 offset:53248
	v_mfma_f32_16x16x32_bf16 v[64:67], v[180:183], v[192:195], v[64:67]
	v_mfma_f32_16x16x32_bf16 v[60:63], v[184:187], v[192:195], v[60:63]
	v_mfma_f32_16x16x32_bf16 v[76:79], v[188:191], v[192:195], v[76:79]
	s_waitcnt lgkmcnt(2)
	v_mfma_f32_16x16x32_bf16 v[68:71], v[176:179], v[208:211], v[68:71]
	ds_read_b128 v[192:195], v199 offset:37888
	buffer_load_dwordx4 v[16:19], v197, s[24:27], s43 offen
	s_waitcnt vmcnt(12)
	v_cvt_pk_bf16_f32 v27, v26, v27
	v_cvt_pk_bf16_f32 v26, v24, v25
	v_mfma_f32_16x16x32_bf16 v[56:59], v[180:183], v[208:211], v[56:59]
	ds_write_b64 v198, v[26:27] offset:26112
	v_mfma_f32_16x16x32_bf16 v[52:55], v[184:187], v[208:211], v[52:55]
	v_mfma_f32_16x16x32_bf16 v[48:51], v[188:191], v[208:211], v[48:51]
	s_waitcnt lgkmcnt(2)
	v_mfma_f32_16x16x32_bf16 v[44:47], v[176:179], v[212:215], v[44:47]
	ds_read_b128 v[176:179], v199 offset:39936
	v_mfma_f32_16x16x32_bf16 v[40:43], v[180:183], v[212:215], v[40:43]
	ds_read_b64_tr_b16 v[244:245], v205 offset:52224
	ds_read_b64_tr_b16 v[248:249], v205 offset:52256
	ds_read_b64_tr_b16 v[216:217], v205 offset:52288
	ds_read_b64_tr_b16 v[220:221], v205 offset:52320
	ds_read_b64_tr_b16 v[246:247], v206 offset:52224
	ds_read_b64_tr_b16 v[250:251], v206 offset:52256
	ds_read_b64_tr_b16 v[218:219], v206 offset:52288
	ds_read_b64_tr_b16 v[222:223], v206 offset:52320
	v_mfma_f32_16x16x32_bf16 v[36:39], v[184:187], v[212:215], v[36:39]
	v_mfma_f32_16x16x32_bf16 v[32:35], v[188:191], v[212:215], v[32:35]
	s_waitcnt lgkmcnt(3)
	v_mfma_f32_16x16x32_bf16 v[172:175], v[244:247], v[192:195], v[172:175]
	ds_read_b128 v[184:187], v199 offset:41984
	buffer_load_dwordx4 v[24:27], v197, s[24:27], s9 offen
	s_waitcnt vmcnt(12)
	v_cvt_pk_bf16_f32 v15, v14, v15
	v_cvt_pk_bf16_f32 v14, v12, v13
	s_waitcnt lgkmcnt(3)
; #define G_ENDTILE(VM) do { asm volatile("s_waitcnt vmcnt(" #VM ")" ::: "memory"); \
;         asm volatile("s_waitcnt lgkmcnt(0)" ::: "memory"); __builtin_amdgcn_s_barrier(); asm volatile("" ::: "memory"); } while (0)
;     ...
;         for (int t = 0; t < nt - 2; t += 2) {
;             G_TILE(G_A0, G_B0, true, G_B1, G_A1, t + 1, true, t + 2, (void)0);
;             G_ENDTILE(8);
;             G_TILE(G_A1, G_B1, true, G_B0, G_A0, t + 2, true, t + 3, (void)0);
;             G_ENDTILE(8);
;         }
	v_mfma_f32_16x16x32_bf16 v[168:171], v[248:251], v[192:195], v[168:171]
	ds_write_b64 v198, v[14:15] offset:256
	s_waitcnt lgkmcnt(3)
	v_mfma_f32_16x16x32_bf16 v[164:167], v[216:219], v[192:195], v[164:167]
	s_waitcnt lgkmcnt(2)
	v_mfma_f32_16x16x32_bf16 v[160:163], v[220:223], v[192:195], v[160:163]
	v_mfma_f32_16x16x32_bf16 v[156:159], v[244:247], v[176:179], v[156:159]
	ds_read_b128 v[188:191], v199 offset:44032
	v_mfma_f32_16x16x32_bf16 v[152:155], v[248:251], v[176:179], v[152:155]
	v_mfma_f32_16x16x32_bf16 v[148:151], v[216:219], v[176:179], v[148:151]
	v_mfma_f32_16x16x32_bf16 v[144:147], v[220:223], v[176:179], v[144:147]
	s_waitcnt lgkmcnt(2)
	v_mfma_f32_16x16x32_bf16 v[132:135], v[244:247], v[184:187], v[132:135]
	ds_read_b128 v[176:179], v199 offset:46080
	buffer_load_dwordx4 v[12:15], v197, s[16:19], s38 offen
	s_waitcnt vmcnt(12)
	v_cvt_pk_bf16_f32 v7, v6, v7
	v_cvt_pk_bf16_f32 v6, v4, v5
	v_mfma_f32_16x16x32_bf16 v[124:127], v[248:251], v[184:187], v[124:127]
	ds_write_b64 v198, v[6:7] offset:8960
	v_mfma_f32_16x16x32_bf16 v[120:123], v[216:219], v[184:187], v[120:123]
	v_mfma_f32_16x16x32_bf16 v[140:143], v[220:223], v[184:187], v[140:143]
	s_waitcnt lgkmcnt(2)
	v_mfma_f32_16x16x32_bf16 v[136:139], v[244:247], v[188:191], v[136:139]
	ds_read_b128 v[184:187], v199 offset:48128
	v_mfma_f32_16x16x32_bf16 v[128:131], v[248:251], v[188:191], v[128:131]
	v_mfma_f32_16x16x32_bf16 v[116:119], v[216:219], v[188:191], v[116:119]
	v_mfma_f32_16x16x32_bf16 v[112:115], v[220:223], v[188:191], v[112:115]
	s_waitcnt lgkmcnt(2)
	v_mfma_f32_16x16x32_bf16 v[100:103], v[244:247], v[176:179], v[100:103]
	ds_read_b128 v[188:191], v199 offset:50176
	buffer_load_dwordx4 v[4:7], v197, s[16:19], s39 offen
	s_waitcnt vmcnt(12)
	v_cvt_pk_bf16_f32 v3, v2, v3
	v_cvt_pk_bf16_f32 v2, v0, v1
	v_mfma_f32_16x16x32_bf16 v[92:95], v[248:251], v[176:179], v[92:95]
	ds_write_b64 v198, v[2:3] offset:17664
	v_mfma_f32_16x16x32_bf16 v[88:91], v[216:219], v[176:179], v[88:91]
	v_mfma_f32_16x16x32_bf16 v[108:111], v[220:223], v[176:179], v[108:111]
	s_waitcnt lgkmcnt(2)
	v_mfma_f32_16x16x32_bf16 v[104:107], v[244:247], v[184:187], v[104:107]
	ds_read_b128 v[176:179], v199 offset:52224
	v_mfma_f32_16x16x32_bf16 v[96:99], v[248:251], v[184:187], v[96:99]
	v_mfma_f32_16x16x32_bf16 v[84:87], v[216:219], v[184:187], v[84:87]
	v_mfma_f32_16x16x32_bf16 v[80:83], v[220:223], v[184:187], v[80:83]
	s_waitcnt lgkmcnt(2)
	v_mfma_f32_16x16x32_bf16 v[72:75], v[244:247], v[188:191], v[72:75]
	ds_read_b128 v[252:255], v199 offset:54272
	buffer_load_dwordx4 v[0:3], v197, s[16:19], s43 offen
	s_waitcnt vmcnt(12)
	v_cvt_pk_bf16_f32 v11, v10, v11
	v_cvt_pk_bf16_f32 v10, v8, v9
	v_mfma_f32_16x16x32_bf16 v[64:67], v[248:251], v[188:191], v[64:67]
	ds_write_b64 v198, v[10:11] offset:26368
	v_mfma_f32_16x16x32_bf16 v[60:63], v[216:219], v[188:191], v[60:63]
	v_mfma_f32_16x16x32_bf16 v[76:79], v[220:223], v[188:191], v[76:79]
	s_waitcnt lgkmcnt(2)
	v_mfma_f32_16x16x32_bf16 v[68:71], v[244:247], v[176:179], v[68:71]
	v_mfma_f32_16x16x32_bf16 v[56:59], v[248:251], v[176:179], v[56:59]
	v_mfma_f32_16x16x32_bf16 v[52:55], v[216:219], v[176:179], v[52:55]
	v_mfma_f32_16x16x32_bf16 v[48:51], v[220:223], v[176:179], v[48:51]
	s_waitcnt lgkmcnt(1)
	buffer_load_dwordx4 v[8:11], v197, s[16:19], s9 offen
	s_waitcnt vmcnt(8)
	s_waitcnt lgkmcnt(0)
	s_barrier
	s_add_i32 s8, s8, 2
	s_add_i32 s9, s9, 0x100000
	s_addk_i32 s36, 0x100
	s_cmp_ge_i32 s8, s84
	s_cbranch_scc0 .LBB0_863
	v_mfma_f32_16x16x32_bf16 v[44:47], v[244:247], v[252:255], v[44:47]
	v_mfma_f32_16x16x32_bf16 v[40:43], v[248:251], v[252:255], v[40:43]
	v_mfma_f32_16x16x32_bf16 v[36:39], v[216:219], v[252:255], v[36:39]
	v_mfma_f32_16x16x32_bf16 v[32:35], v[220:223], v[252:255], v[32:35]
	s_branch .LBB0_865

.Lchk6_s2:
	buffer_load_dwordx4 v201, s[20:23], s38 offen lds
	s_waitcnt vmcnt(9)
	s_cmp_le_u32 s99, 1
	s_cbranch_scc1 .Lchk6_s3
	v_mfma_f32_16x16x32_bf16 v[156:159], v[176:179], v[208:211], v[156:159]
	v_mfma_f32_16x16x32_bf16 v[152:155], v[180:183], v[208:211], v[152:155]
	v_mfma_f32_16x16x32_bf16 v[148:151], v[184:187], v[208:211], v[148:151]
	v_mfma_f32_16x16x32_bf16 v[144:147], v[188:191], v[208:211], v[144:147]
.Lchk6_s3:
	s_mov_b32 m0, s87
	s_nop 0
	buffer_load_dwordx4 v202, s[20:23], s38 offen lds
	ds_read_b128 v[192:195], v199 offset:6144
	v_cvt_pk_bf16_f32 v23, v22, v23
	v_cvt_pk_bf16_f32 v22, v20, v21
	ds_write_b64 v198, v[22:23] offset:34816
	s_mov_b32 m0, s88
	s_nop 0
	buffer_load_dwordx4 v203, s[20:23], s38 offen lds
	s_cmp_le_u32 s99, 2
	s_cbranch_scc1 .Lchk6_s4
	v_mfma_f32_16x16x32_bf16 v[132:135], v[176:179], v[212:215], v[132:135]
	v_mfma_f32_16x16x32_bf16 v[124:127], v[180:183], v[212:215], v[124:127]
	v_mfma_f32_16x16x32_bf16 v[120:123], v[184:187], v[212:215], v[120:123]
	v_mfma_f32_16x16x32_bf16 v[140:143], v[188:191], v[212:215], v[140:143]
.Lchk6_s4:
	s_mov_b32 m0, s89
	s_nop 0
	buffer_load_dwordx4 v204, s[20:23], s38 offen lds
	s_add_i32 s38, s9, 0xfff20000
	ds_read_b128 v[208:211], v199 offset:8192
	s_waitcnt lgkmcnt(2)
	s_waitcnt vmcnt(10)
	s_cmp_le_u32 s99, 3
	s_cbranch_scc1 .Lchk6_s5
	v_mfma_f32_16x16x32_bf16 v[136:139], v[176:179], v[192:195], v[136:139]
	v_mfma_f32_16x16x32_bf16 v[128:131], v[180:183], v[192:195], v[128:131]
	v_mfma_f32_16x16x32_bf16 v[116:119], v[184:187], v[192:195], v[116:119]
	v_mfma_f32_16x16x32_bf16 v[112:115], v[188:191], v[192:195], v[112:115]

.Lchk6_s20:
	buffer_load_dwordx4 v201, s[20:23], s36 offen lds
	s_add_i32 s38, s9, 0xfffa0000
	s_waitcnt lgkmcnt(1)
	s_waitcnt vmcnt(9)
	s_cmp_le_u32 s99, 1
	s_cbranch_scc1 .Lchk6_s21
	v_mfma_f32_16x16x32_bf16 v[156:159], v[176:179], v[208:211], v[156:159]
	v_mfma_f32_16x16x32_bf16 v[152:155], v[180:183], v[208:211], v[152:155]
	v_mfma_f32_16x16x32_bf16 v[148:151], v[184:187], v[208:211], v[148:151]
	v_mfma_f32_16x16x32_bf16 v[144:147], v[188:191], v[208:211], v[144:147]
.Lchk6_s21:
	s_mov_b32 m0, s77
	s_nop 0
	buffer_load_dwordx4 v202, s[20:23], s36 offen lds
	ds_read_b128 v[192:195], v199 offset:43008
	v_cvt_pk_bf16_f32 v23, v22, v23
	v_cvt_pk_bf16_f32 v22, v20, v21
	ds_write_b64 v198, v[22:23]
	s_mov_b32 m0, s78
	s_nop 0
	buffer_load_dwordx4 v203, s[20:23], s36 offen lds
	s_waitcnt lgkmcnt(2)
	s_cmp_le_u32 s99, 2
	s_cbranch_scc1 .Lchk6_s22
	v_mfma_f32_16x16x32_bf16 v[132:135], v[176:179], v[212:215], v[132:135]
	v_mfma_f32_16x16x32_bf16 v[124:127], v[180:183], v[212:215], v[124:127]
	v_mfma_f32_16x16x32_bf16 v[120:123], v[184:187], v[212:215], v[120:123]
	v_mfma_f32_16x16x32_bf16 v[140:143], v[188:191], v[212:215], v[140:143]
.Lchk6_s22:
	s_mov_b32 m0, s79
	s_nop 0
	buffer_load_dwordx4 v204, s[20:23], s36 offen lds
	ds_read_b128 v[208:211], v199 offset:45056
	s_waitcnt lgkmcnt(2)
	s_waitcnt vmcnt(11)
	s_cmp_le_u32 s99, 3
	s_cbranch_scc1 .Lchk6_s23
	v_mfma_f32_16x16x32_bf16 v[136:139], v[176:179], v[192:195], v[136:139]
	v_mfma_f32_16x16x32_bf16 v[128:131], v[180:183], v[192:195], v[128:131]
	v_mfma_f32_16x16x32_bf16 v[116:119], v[184:187], v[192:195], v[116:119]
	v_mfma_f32_16x16x32_bf16 v[112:115], v[188:191], v[192:195], v[112:115]

; #define G_ENDTILE(VM) do { asm volatile("s_waitcnt vmcnt(" #VM ")" ::: "memory"); \
;         asm volatile("s_waitcnt lgkmcnt(0)" ::: "memory"); __builtin_amdgcn_s_barrier(); asm volatile("" ::: "memory"); } while (0)
;     ...
;         for (int t = 0; t < nt - 2; t += 2) {
;             G_TILE(G_A0, G_B0, true, G_B1, G_A1, t + 1, true, t + 2, (void)0);
;             G_ENDTILE(8);
.LBB0_899:
	s_mov_b32 m0, s64
	s_add_i32 s69, s45, 0xffffff80
	ds_read_b64_tr_b16 v[170:171], v166
	ds_read_b64_tr_b16 v[172:173], v167
	ds_read_b64_tr_b16 v[176:177], v167 offset:32
	ds_read_b128 v[178:181], v162
	ds_read_b64_tr_b16 v[174:175], v166 offset:32
	ds_read_b64_tr_b16 v[182:183], v166 offset:64
	ds_read_b64_tr_b16 v[186:187], v166 offset:96
	ds_read_b64_tr_b16 v[184:185], v167 offset:64
	ds_read_b64_tr_b16 v[188:189], v167 offset:96
	ds_read_b128 v[190:193], v162 offset:2048
	ds_read_b128 v[198:201], v162 offset:4096
	buffer_load_dwordx4 v163, s[20:23], s69 offen lds
	s_mov_b32 m0, s63
	v_mfma_f32_16x16x32_bf16 v[44:47], v[244:247], v[252:255], v[44:47]
	v_mfma_f32_16x16x32_bf16 v[40:43], v[248:251], v[252:255], v[40:43]
	v_mfma_f32_16x16x32_bf16 v[36:39], v[202:205], v[252:255], v[36:39]
	v_mfma_f32_16x16x32_bf16 v[32:35], v[206:209], v[252:255], v[32:35]
	s_waitcnt lgkmcnt(7)
	v_mfma_f32_16x16x32_bf16 v[156:159], v[170:173], v[178:181], v[156:159]
	buffer_load_dwordx4 v165, s[20:23], s69 offen lds
	s_waitcnt lgkmcnt(6)
	v_mfma_f32_16x16x32_bf16 v[152:155], v[174:177], v[178:181], v[152:155]
	s_waitcnt lgkmcnt(3)
	v_mfma_f32_16x16x32_bf16 v[148:151], v[182:185], v[178:181], v[148:151]
	s_waitcnt lgkmcnt(2)
	v_mfma_f32_16x16x32_bf16 v[144:147], v[186:189], v[178:181], v[144:147]
	s_waitcnt lgkmcnt(1)
	v_mfma_f32_16x16x32_bf16 v[140:143], v[170:173], v[190:193], v[140:143]
	s_mov_b32 m0, s62
	s_nop 0
	buffer_load_dwordx4 v164, s[20:23], s69 offen lds
	ds_read_b128 v[178:181], v162 offset:6144
	s_waitcnt vmcnt(10)
	v_cvt_pk_bf16_f32 v15, v14, v15
	v_cvt_pk_bf16_f32 v14, v12, v13
	v_mfma_f32_16x16x32_bf16 v[136:139], v[174:177], v[190:193], v[136:139]
	ds_write_b64 v161, v[14:15] offset:34816
	v_mfma_f32_16x16x32_bf16 v[132:135], v[182:185], v[190:193], v[132:135]
	s_mov_b32 m0, s31
	s_nop 0
	buffer_load_dwordx4 v168, s[20:23], s69 offen lds
	s_add_i32 s69, s13, 0xfff20000
	v_mfma_f32_16x16x32_bf16 v[128:131], v[186:189], v[190:193], v[128:131]
	s_waitcnt lgkmcnt(2)
	v_mfma_f32_16x16x32_bf16 v[124:127], v[170:173], v[198:201], v[124:127]
	ds_read_b128 v[190:193], v162 offset:8192
	v_mfma_f32_16x16x32_bf16 v[120:123], v[174:177], v[198:201], v[120:123]
	v_mfma_f32_16x16x32_bf16 v[116:119], v[182:185], v[198:201], v[116:119]
	v_mfma_f32_16x16x32_bf16 v[112:115], v[186:189], v[198:201], v[112:115]
	s_waitcnt lgkmcnt(2)
	v_mfma_f32_16x16x32_bf16 v[108:111], v[170:173], v[178:181], v[108:111]
	ds_read_b128 v[198:201], v162 offset:10240
	buffer_load_dwordx4 v[12:15], v160, s[24:27], s69 offen
	s_waitcnt vmcnt(11)
	v_cvt_pk_bf16_f32 v3, v2, v3
	v_cvt_pk_bf16_f32 v2, v0, v1
	v_mfma_f32_16x16x32_bf16 v[104:107], v[174:177], v[178:181], v[104:107]
	ds_write_b64 v161, v[2:3] offset:43520
	v_mfma_f32_16x16x32_bf16 v[100:103], v[182:185], v[178:181], v[100:103]
	v_mfma_f32_16x16x32_bf16 v[96:99], v[186:189], v[178:181], v[96:99]
	s_add_i32 s74, s13, 0xfff40000
	s_waitcnt lgkmcnt(2)
	v_mfma_f32_16x16x32_bf16 v[92:95], v[170:173], v[190:193], v[92:95]
	ds_read_b128 v[178:181], v162 offset:12288
	v_mfma_f32_16x16x32_bf16 v[88:91], v[174:177], v[190:193], v[88:91]
	v_mfma_f32_16x16x32_bf16 v[84:87], v[182:185], v[190:193], v[84:87]
	v_mfma_f32_16x16x32_bf16 v[80:83], v[186:189], v[190:193], v[80:83]
	s_waitcnt lgkmcnt(2)
	v_mfma_f32_16x16x32_bf16 v[76:79], v[170:173], v[198:201], v[76:79]
	ds_read_b128 v[190:193], v162 offset:14336
	buffer_load_dwordx4 v[0:3], v160, s[24:27], s74 offen
	s_waitcnt vmcnt(11)
	v_cvt_pk_bf16_f32 v31, v30, v31
	v_cvt_pk_bf16_f32 v30, v28, v29
	v_mfma_f32_16x16x32_bf16 v[72:75], v[174:177], v[198:201], v[72:75]
	ds_write_b64 v161, v[30:31] offset:52224
	v_mfma_f32_16x16x32_bf16 v[68:71], v[182:185], v[198:201], v[68:71]
	v_mfma_f32_16x16x32_bf16 v[64:67], v[186:189], v[198:201], v[64:67]
	s_add_i32 s75, s13, 0xfff60000
	s_waitcnt lgkmcnt(2)
	v_mfma_f32_16x16x32_bf16 v[60:63], v[170:173], v[178:181], v[60:63]
	ds_read_b128 v[198:201], v162 offset:1024
	v_mfma_f32_16x16x32_bf16 v[56:59], v[174:177], v[178:181], v[56:59]
	v_mfma_f32_16x16x32_bf16 v[52:55], v[182:185], v[178:181], v[52:55]
	v_mfma_f32_16x16x32_bf16 v[48:51], v[186:189], v[178:181], v[48:51]
	s_waitcnt lgkmcnt(2)
	v_mfma_f32_16x16x32_bf16 v[44:47], v[170:173], v[190:193], v[44:47]
	ds_read_b128 v[170:173], v162 offset:3072
	buffer_load_dwordx4 v[28:31], v160, s[24:27], s75 offen
	s_waitcnt vmcnt(11)
	v_cvt_pk_bf16_f32 v27, v26, v27
	v_cvt_pk_bf16_f32 v26, v24, v25
	v_mfma_f32_16x16x32_bf16 v[40:43], v[174:177], v[190:193], v[40:43]
	ds_read_b64_tr_b16 v[244:245], v166 offset:17408
	ds_read_b64_tr_b16 v[248:249], v166 offset:17440
	ds_read_b64_tr_b16 v[202:203], v166 offset:17472
	ds_read_b64_tr_b16 v[206:207], v166 offset:17504
	ds_read_b64_tr_b16 v[246:247], v167 offset:17408
	ds_read_b64_tr_b16 v[250:251], v167 offset:17440
	ds_read_b64_tr_b16 v[204:205], v167 offset:17472
	ds_read_b64_tr_b16 v[208:209], v167 offset:17504
	ds_write_b64 v161, v[26:27] offset:60928
	v_mfma_f32_16x16x32_bf16 v[36:39], v[182:185], v[190:193], v[36:39]
	v_mfma_f32_16x16x32_bf16 v[32:35], v[186:189], v[190:193], v[32:35]
	s_add_i32 s76, s13, 0xfff80000
	s_waitcnt lgkmcnt(4)
	v_mfma_f32_16x16x32_bf16 v[156:159], v[244:247], v[198:201], v[156:159]
	ds_read_b128 v[182:185], v162 offset:5120
	s_waitcnt lgkmcnt(4)
	v_mfma_f32_16x16x32_bf16 v[152:155], v[248:251], v[198:201], v[152:155]
	s_waitcnt lgkmcnt(3)
	v_mfma_f32_16x16x32_bf16 v[148:151], v[202:205], v[198:201], v[148:151]
	s_waitcnt lgkmcnt(2)
	v_mfma_f32_16x16x32_bf16 v[144:147], v[206:209], v[198:201], v[144:147]
	v_mfma_f32_16x16x32_bf16 v[140:143], v[244:247], v[170:173], v[140:143]
	ds_read_b128 v[186:189], v162 offset:7168
	buffer_load_dwordx4 v[24:27], v160, s[24:27], s76 offen
	s_waitcnt vmcnt(11)
; #define G_ENDTILE(VM) do { asm volatile("s_waitcnt vmcnt(" #VM ")" ::: "memory"); \
;         asm volatile("s_waitcnt lgkmcnt(0)" ::: "memory"); __builtin_amdgcn_s_barrier(); asm volatile("" ::: "memory"); } while (0)
;     ...
;         for (int t = 0; t < nt - 2; t += 2) {
;             G_TILE(G_A0, G_B0, true, G_B1, G_A1, t + 1, true, t + 2, (void)0);
;             G_ENDTILE(8);
;             G_TILE(G_A1, G_B1, true, G_B0, G_A0, t + 2, true, t + 3, (void)0);
;             G_ENDTILE(8);
	v_cvt_pk_bf16_f32 v23, v22, v23
	v_cvt_pk_bf16_f32 v22, v20, v21
	v_mfma_f32_16x16x32_bf16 v[136:139], v[248:251], v[170:173], v[136:139]
	ds_write_b64 v161, v[22:23] offset:35072
	v_mfma_f32_16x16x32_bf16 v[132:135], v[202:205], v[170:173], v[132:135]
	v_mfma_f32_16x16x32_bf16 v[128:131], v[206:209], v[170:173], v[128:131]
	s_waitcnt lgkmcnt(2)
	v_mfma_f32_16x16x32_bf16 v[124:127], v[244:247], v[182:185], v[124:127]
	ds_read_b128 v[170:173], v162 offset:9216
	v_mfma_f32_16x16x32_bf16 v[120:123], v[248:251], v[182:185], v[120:123]
	v_mfma_f32_16x16x32_bf16 v[116:119], v[202:205], v[182:185], v[116:119]
	v_mfma_f32_16x16x32_bf16 v[112:115], v[206:209], v[182:185], v[112:115]
	s_waitcnt lgkmcnt(2)
	v_mfma_f32_16x16x32_bf16 v[108:111], v[244:247], v[186:189], v[108:111]
	ds_read_b128 v[182:185], v162 offset:11264
	buffer_load_dwordx4 v[20:23], v160, s[16:19], s69 offen
	s_waitcnt vmcnt(11)
	v_cvt_pk_bf16_f32 v7, v6, v7
	v_cvt_pk_bf16_f32 v6, v4, v5
	v_mfma_f32_16x16x32_bf16 v[104:107], v[248:251], v[186:189], v[104:107]
	ds_write_b64 v161, v[6:7] offset:43776
	v_mfma_f32_16x16x32_bf16 v[100:103], v[202:205], v[186:189], v[100:103]
	v_mfma_f32_16x16x32_bf16 v[96:99], v[206:209], v[186:189], v[96:99]
	s_waitcnt lgkmcnt(2)
	v_mfma_f32_16x16x32_bf16 v[92:95], v[244:247], v[170:173], v[92:95]
	ds_read_b128 v[186:189], v162 offset:13312
	v_mfma_f32_16x16x32_bf16 v[88:91], v[248:251], v[170:173], v[88:91]
	v_mfma_f32_16x16x32_bf16 v[84:87], v[202:205], v[170:173], v[84:87]
	v_mfma_f32_16x16x32_bf16 v[80:83], v[206:209], v[170:173], v[80:83]
	s_waitcnt lgkmcnt(2)
	v_mfma_f32_16x16x32_bf16 v[76:79], v[244:247], v[182:185], v[76:79]
	ds_read_b128 v[252:255], v162 offset:15360
	buffer_load_dwordx4 v[4:7], v160, s[16:19], s74 offen
	s_waitcnt vmcnt(11)
	v_cvt_pk_bf16_f32 v11, v10, v11
	v_cvt_pk_bf16_f32 v10, v8, v9
	v_mfma_f32_16x16x32_bf16 v[72:75], v[248:251], v[182:185], v[72:75]
	ds_write_b64 v161, v[10:11] offset:52480
	v_mfma_f32_16x16x32_bf16 v[68:71], v[202:205], v[182:185], v[68:71]
	v_mfma_f32_16x16x32_bf16 v[64:67], v[206:209], v[182:185], v[64:67]
	s_waitcnt lgkmcnt(2)
	v_mfma_f32_16x16x32_bf16 v[60:63], v[244:247], v[186:189], v[60:63]
	v_mfma_f32_16x16x32_bf16 v[56:59], v[248:251], v[186:189], v[56:59]
	v_mfma_f32_16x16x32_bf16 v[52:55], v[202:205], v[186:189], v[52:55]
	v_mfma_f32_16x16x32_bf16 v[48:51], v[206:209], v[186:189], v[48:51]
	s_waitcnt lgkmcnt(1)
	buffer_load_dwordx4 v[8:11], v160, s[16:19], s75 offen
	s_waitcnt vmcnt(11)
	v_cvt_pk_bf16_f32 v19, v18, v19
	v_cvt_pk_bf16_f32 v18, v16, v17
	ds_write_b64 v161, v[18:19] offset:61184
	buffer_load_dwordx4 v[16:19], v160, s[16:19], s76 offen
	s_waitcnt vmcnt(8)
	s_mov_b32 m0, s56
	s_waitcnt lgkmcnt(0)
	s_barrier
	ds_read_b64_tr_b16 v[170:171], v166 offset:34816
	ds_read_b64_tr_b16 v[172:173], v167 offset:34816
	ds_read_b64_tr_b16 v[176:177], v167 offset:34848
	ds_read_b128 v[178:181], v162 offset:32768
	ds_read_b64_tr_b16 v[174:175], v166 offset:34848
	ds_read_b64_tr_b16 v[182:183], v166 offset:34880
	ds_read_b64_tr_b16 v[186:187], v166 offset:34912
	ds_read_b64_tr_b16 v[184:185], v167 offset:34880
	ds_read_b64_tr_b16 v[188:189], v167 offset:34912
	ds_read_b128 v[190:193], v162 offset:34816
	ds_read_b128 v[198:201], v162 offset:36864
	buffer_load_dwordx4 v163, s[20:23], s45 offen lds
	s_mov_b32 m0, s57
	v_mfma_f32_16x16x32_bf16 v[44:47], v[244:247], v[252:255], v[44:47]
	v_mfma_f32_16x16x32_bf16 v[40:43], v[248:251], v[252:255], v[40:43]
	v_mfma_f32_16x16x32_bf16 v[36:39], v[202:205], v[252:255], v[36:39]
	v_mfma_f32_16x16x32_bf16 v[32:35], v[206:209], v[252:255], v[32:35]
	s_waitcnt lgkmcnt(7)
	v_mfma_f32_16x16x32_bf16 v[156:159], v[170:173], v[178:181], v[156:159]
	buffer_load_dwordx4 v165, s[20:23], s45 offen lds
	s_add_i32 s69, s13, 0xfffa0000
	s_waitcnt lgkmcnt(6)
	v_mfma_f32_16x16x32_bf16 v[152:155], v[174:177], v[178:181], v[152:155]
	s_waitcnt lgkmcnt(3)
	v_mfma_f32_16x16x32_bf16 v[148:151], v[182:185], v[178:181], v[148:151]
	s_waitcnt lgkmcnt(2)
	v_mfma_f32_16x16x32_bf16 v[144:147], v[186:189], v[178:181], v[144:147]
	s_waitcnt lgkmcnt(1)
	v_mfma_f32_16x16x32_bf16 v[140:143], v[170:173], v[190:193], v[140:143]
	s_mov_b32 m0, s58
	s_nop 0
	buffer_load_dwordx4 v164, s[20:23], s45 offen lds
	ds_read_b128 v[178:181], v162 offset:38912
	s_waitcnt vmcnt(10)
	v_cvt_pk_bf16_f32 v15, v14, v15
	v_cvt_pk_bf16_f32 v14, v12, v13
	v_mfma_f32_16x16x32_bf16 v[136:139], v[174:177], v[190:193], v[136:139]
	ds_write_b64 v161, v[14:15]
	v_mfma_f32_16x16x32_bf16 v[132:135], v[182:185], v[190:193], v[132:135]
	s_mov_b32 m0, s59
	s_nop 0
	buffer_load_dwordx4 v168, s[20:23], s45 offen lds
	v_mfma_f32_16x16x32_bf16 v[128:131], v[186:189], v[190:193], v[128:131]
	s_waitcnt lgkmcnt(2)
	v_mfma_f32_16x16x32_bf16 v[124:127], v[170:173], v[198:201], v[124:127]
	ds_read_b128 v[190:193], v162 offset:40960
	v_mfma_f32_16x16x32_bf16 v[120:123], v[174:177], v[198:201], v[120:123]
	v_mfma_f32_16x16x32_bf16 v[116:119], v[182:185], v[198:201], v[116:119]
	v_mfma_f32_16x16x32_bf16 v[112:115], v[186:189], v[198:201], v[112:115]
	s_waitcnt lgkmcnt(2)
	v_mfma_f32_16x16x32_bf16 v[108:111], v[170:173], v[178:181], v[108:111]
	ds_read_b128 v[198:201], v162 offset:43008
	buffer_load_dwordx4 v[12:15], v160, s[24:27], s69 offen
	s_waitcnt vmcnt(11)
	v_cvt_pk_bf16_f32 v3, v2, v3
	v_cvt_pk_bf16_f32 v2, v0, v1
	v_mfma_f32_16x16x32_bf16 v[104:107], v[174:177], v[178:181], v[104:107]
	ds_write_b64 v161, v[2:3] offset:8704
	v_mfma_f32_16x16x32_bf16 v[100:103], v[182:185], v[178:181], v[100:103]
	v_mfma_f32_16x16x32_bf16 v[96:99], v[186:189], v[178:181], v[96:99]
	s_add_i32 s74, s13, 0xfffc0000
	s_waitcnt lgkmcnt(2)
; #define G_ENDTILE(VM) do { asm volatile("s_waitcnt vmcnt(" #VM ")" ::: "memory"); \
;         asm volatile("s_waitcnt lgkmcnt(0)" ::: "memory"); __builtin_amdgcn_s_barrier(); asm volatile("" ::: "memory"); } while (0)
;     ...
;         for (int t = 0; t < nt - 2; t += 2) {
;             G_TILE(G_A0, G_B0, true, G_B1, G_A1, t + 1, true, t + 2, (void)0);
;             G_ENDTILE(8);
;             G_TILE(G_A1, G_B1, true, G_B0, G_A0, t + 2, true, t + 3, (void)0);
;             G_ENDTILE(8);
;         }
	v_mfma_f32_16x16x32_bf16 v[92:95], v[170:173], v[190:193], v[92:95]
	ds_read_b128 v[178:181], v162 offset:45056
	v_mfma_f32_16x16x32_bf16 v[88:91], v[174:177], v[190:193], v[88:91]
	v_mfma_f32_16x16x32_bf16 v[84:87], v[182:185], v[190:193], v[84:87]
	v_mfma_f32_16x16x32_bf16 v[80:83], v[186:189], v[190:193], v[80:83]
	s_waitcnt lgkmcnt(2)
	v_mfma_f32_16x16x32_bf16 v[76:79], v[170:173], v[198:201], v[76:79]
	ds_read_b128 v[190:193], v162 offset:47104
	buffer_load_dwordx4 v[0:3], v160, s[24:27], s74 offen
	s_waitcnt vmcnt(11)
	v_cvt_pk_bf16_f32 v31, v30, v31
	v_cvt_pk_bf16_f32 v30, v28, v29
	v_mfma_f32_16x16x32_bf16 v[72:75], v[174:177], v[198:201], v[72:75]
	ds_write_b64 v161, v[30:31] offset:17408
	v_mfma_f32_16x16x32_bf16 v[68:71], v[182:185], v[198:201], v[68:71]
	v_mfma_f32_16x16x32_bf16 v[64:67], v[186:189], v[198:201], v[64:67]
	s_add_i32 s75, s13, 0xfffe0000
	s_waitcnt lgkmcnt(2)
	v_mfma_f32_16x16x32_bf16 v[60:63], v[170:173], v[178:181], v[60:63]
	ds_read_b128 v[198:201], v162 offset:33792
	v_mfma_f32_16x16x32_bf16 v[56:59], v[174:177], v[178:181], v[56:59]
	v_mfma_f32_16x16x32_bf16 v[52:55], v[182:185], v[178:181], v[52:55]
	v_mfma_f32_16x16x32_bf16 v[48:51], v[186:189], v[178:181], v[48:51]
	s_waitcnt lgkmcnt(2)
	v_mfma_f32_16x16x32_bf16 v[44:47], v[170:173], v[190:193], v[44:47]
	ds_read_b128 v[170:173], v162 offset:35840
	buffer_load_dwordx4 v[28:31], v160, s[24:27], s75 offen
	s_waitcnt vmcnt(11)
	v_cvt_pk_bf16_f32 v27, v26, v27
	v_cvt_pk_bf16_f32 v26, v24, v25
	v_mfma_f32_16x16x32_bf16 v[40:43], v[174:177], v[190:193], v[40:43]
	ds_read_b64_tr_b16 v[244:245], v166 offset:52224
	ds_read_b64_tr_b16 v[248:249], v166 offset:52256
	ds_read_b64_tr_b16 v[202:203], v166 offset:52288
	ds_read_b64_tr_b16 v[206:207], v166 offset:52320
	ds_read_b64_tr_b16 v[246:247], v167 offset:52224
	ds_read_b64_tr_b16 v[250:251], v167 offset:52256
	ds_read_b64_tr_b16 v[204:205], v167 offset:52288
	ds_read_b64_tr_b16 v[208:209], v167 offset:52320
	ds_write_b64 v161, v[26:27] offset:26112
	v_mfma_f32_16x16x32_bf16 v[36:39], v[182:185], v[190:193], v[36:39]
	v_mfma_f32_16x16x32_bf16 v[32:35], v[186:189], v[190:193], v[32:35]
	s_waitcnt lgkmcnt(4)
	v_mfma_f32_16x16x32_bf16 v[156:159], v[244:247], v[198:201], v[156:159]
	ds_read_b128 v[182:185], v162 offset:37888
	s_waitcnt lgkmcnt(4)
	v_mfma_f32_16x16x32_bf16 v[152:155], v[248:251], v[198:201], v[152:155]
	s_waitcnt lgkmcnt(3)
	v_mfma_f32_16x16x32_bf16 v[148:151], v[202:205], v[198:201], v[148:151]
	s_waitcnt lgkmcnt(2)
	v_mfma_f32_16x16x32_bf16 v[144:147], v[206:209], v[198:201], v[144:147]
	v_mfma_f32_16x16x32_bf16 v[140:143], v[244:247], v[170:173], v[140:143]
	ds_read_b128 v[186:189], v162 offset:39936
	buffer_load_dwordx4 v[24:27], v160, s[24:27], s13 offen
	s_waitcnt vmcnt(11)
	v_cvt_pk_bf16_f32 v23, v22, v23
	v_cvt_pk_bf16_f32 v22, v20, v21
	v_mfma_f32_16x16x32_bf16 v[136:139], v[248:251], v[170:173], v[136:139]
	ds_write_b64 v161, v[22:23] offset:256
	v_mfma_f32_16x16x32_bf16 v[132:135], v[202:205], v[170:173], v[132:135]
	v_mfma_f32_16x16x32_bf16 v[128:131], v[206:209], v[170:173], v[128:131]
	s_waitcnt lgkmcnt(2)
	v_mfma_f32_16x16x32_bf16 v[124:127], v[244:247], v[182:185], v[124:127]
	ds_read_b128 v[170:173], v162 offset:41984
	v_mfma_f32_16x16x32_bf16 v[120:123], v[248:251], v[182:185], v[120:123]
	v_mfma_f32_16x16x32_bf16 v[116:119], v[202:205], v[182:185], v[116:119]
	v_mfma_f32_16x16x32_bf16 v[112:115], v[206:209], v[182:185], v[112:115]
	s_waitcnt lgkmcnt(2)
	v_mfma_f32_16x16x32_bf16 v[108:111], v[244:247], v[186:189], v[108:111]
	ds_read_b128 v[182:185], v162 offset:44032
	buffer_load_dwordx4 v[20:23], v160, s[16:19], s69 offen
	s_waitcnt vmcnt(11)
	v_cvt_pk_bf16_f32 v7, v6, v7
	v_cvt_pk_bf16_f32 v6, v4, v5
	v_mfma_f32_16x16x32_bf16 v[104:107], v[248:251], v[186:189], v[104:107]
	ds_write_b64 v161, v[6:7] offset:8960
	v_mfma_f32_16x16x32_bf16 v[100:103], v[202:205], v[186:189], v[100:103]
	v_mfma_f32_16x16x32_bf16 v[96:99], v[206:209], v[186:189], v[96:99]
	s_waitcnt lgkmcnt(2)
	v_mfma_f32_16x16x32_bf16 v[92:95], v[244:247], v[170:173], v[92:95]
	ds_read_b128 v[186:189], v162 offset:46080
	v_mfma_f32_16x16x32_bf16 v[88:91], v[248:251], v[170:173], v[88:91]
	v_mfma_f32_16x16x32_bf16 v[84:87], v[202:205], v[170:173], v[84:87]
	v_mfma_f32_16x16x32_bf16 v[80:83], v[206:209], v[170:173], v[80:83]
	s_waitcnt lgkmcnt(2)
	v_mfma_f32_16x16x32_bf16 v[76:79], v[244:247], v[182:185], v[76:79]
	ds_read_b128 v[252:255], v162 offset:48128
	buffer_load_dwordx4 v[4:7], v160, s[16:19], s74 offen
	s_waitcnt vmcnt(11)
	v_cvt_pk_bf16_f32 v11, v10, v11
	v_cvt_pk_bf16_f32 v10, v8, v9
	v_mfma_f32_16x16x32_bf16 v[72:75], v[248:251], v[182:185], v[72:75]
	ds_write_b64 v161, v[10:11] offset:17664
	v_mfma_f32_16x16x32_bf16 v[68:71], v[202:205], v[182:185], v[68:71]
	v_mfma_f32_16x16x32_bf16 v[64:67], v[206:209], v[182:185], v[64:67]
	s_waitcnt lgkmcnt(2)
	v_mfma_f32_16x16x32_bf16 v[60:63], v[244:247], v[186:189], v[60:63]
	v_mfma_f32_16x16x32_bf16 v[56:59], v[248:251], v[186:189], v[56:59]
	v_mfma_f32_16x16x32_bf16 v[52:55], v[202:205], v[186:189], v[52:55]
	v_mfma_f32_16x16x32_bf16 v[48:51], v[206:209], v[186:189], v[48:51]
	s_waitcnt lgkmcnt(1)
	buffer_load_dwordx4 v[8:11], v160, s[16:19], s75 offen
	s_waitcnt vmcnt(11)
	v_cvt_pk_bf16_f32 v19, v18, v19
	v_cvt_pk_bf16_f32 v18, v16, v17
	ds_write_b64 v161, v[18:19] offset:26368
	buffer_load_dwordx4 v[16:19], v160, s[16:19], s13 offen
	s_waitcnt vmcnt(8)
	s_waitcnt lgkmcnt(0)
	s_barrier
	s_add_i32 s12, s12, 2
	s_add_i32 s13, s13, 0x100000
	s_addk_i32 s45, 0x100
	s_cmp_ge_i32 s12, s30
	s_cbranch_scc0 .LBB0_899
	v_mfma_f32_16x16x32_bf16 v[44:47], v[244:247], v[252:255], v[44:47]
	v_mfma_f32_16x16x32_bf16 v[40:43], v[248:251], v[252:255], v[40:43]
	v_mfma_f32_16x16x32_bf16 v[36:39], v[202:205], v[252:255], v[36:39]
	v_mfma_f32_16x16x32_bf16 v[32:35], v[206:209], v[252:255], v[32:35]
	s_branch .LBB0_901

; #define G_ENDTILE(VM) do { asm volatile("s_waitcnt vmcnt(" #VM ")" ::: "memory"); \
;         asm volatile("s_waitcnt lgkmcnt(0)" ::: "memory"); __builtin_amdgcn_s_barrier(); asm volatile("" ::: "memory"); } while (0)
;     ...
;         for (int t = 0; t < nt - 2; t += 2) {
;             G_TILE(G_A0, G_B0, true, G_B1, G_A1, t + 1, true, t + 2, (void)0);
;             G_ENDTILE(8);
.LBB0_1038:
	s_mov_b32 m0, s64
	s_add_i32 s5, s4, 0xffffff80
	ds_read_b64_tr_b16 v[160:161], v178
	ds_read_b64_tr_b16 v[162:163], v179
	ds_read_b64_tr_b16 v[166:167], v179 offset:32
	ds_read_b128 v[168:171], v175
	ds_read_b64_tr_b16 v[164:165], v178 offset:32
	ds_read_b64_tr_b16 v[182:183], v178 offset:64
	ds_read_b64_tr_b16 v[186:187], v178 offset:96
	ds_read_b64_tr_b16 v[184:185], v179 offset:64
	ds_read_b64_tr_b16 v[188:189], v179 offset:96
	ds_read_b128 v[190:193], v175 offset:2048
	ds_read_b128 v[194:197], v175 offset:4096
	buffer_load_dwordx4 v176, s[16:19], s5 offen lds
	s_mov_b32 m0, s63
	v_mfma_f32_16x16x32_bf16 v[44:47], v[244:247], v[252:255], v[44:47]
	v_mfma_f32_16x16x32_bf16 v[40:43], v[248:251], v[252:255], v[40:43]
	v_mfma_f32_16x16x32_bf16 v[36:39], v[198:201], v[252:255], v[36:39]
	v_mfma_f32_16x16x32_bf16 v[32:35], v[202:205], v[252:255], v[32:35]
	s_waitcnt lgkmcnt(7)
	v_mfma_f32_16x16x32_bf16 v[156:159], v[160:163], v[168:171], v[156:159]
	buffer_load_dwordx4 v177, s[16:19], s5 offen lds
	s_waitcnt lgkmcnt(6)
	v_mfma_f32_16x16x32_bf16 v[152:155], v[164:167], v[168:171], v[152:155]
	s_waitcnt lgkmcnt(3)
	v_mfma_f32_16x16x32_bf16 v[148:151], v[182:185], v[168:171], v[148:151]
	s_waitcnt lgkmcnt(2)
	v_mfma_f32_16x16x32_bf16 v[144:147], v[186:189], v[168:171], v[144:147]
	s_waitcnt lgkmcnt(1)
	v_mfma_f32_16x16x32_bf16 v[140:143], v[160:163], v[190:193], v[140:143]
	s_mov_b32 m0, s62
	s_nop 0
	buffer_load_dwordx4 v180, s[16:19], s5 offen lds
	ds_read_b128 v[168:171], v175 offset:6144
	s_waitcnt vmcnt(10)
	v_cvt_pk_bf16_f32 v15, v14, v15
	v_cvt_pk_bf16_f32 v14, v12, v13
	v_mfma_f32_16x16x32_bf16 v[136:139], v[164:167], v[190:193], v[136:139]
	ds_write_b64 v174, v[14:15] offset:34816
	v_mfma_f32_16x16x32_bf16 v[132:135], v[182:185], v[190:193], v[132:135]
	s_mov_b32 m0, s61
	s_nop 0
	buffer_load_dwordx4 v181, s[16:19], s5 offen lds
	s_add_i32 s5, s1, 0xfff20000
	v_mfma_f32_16x16x32_bf16 v[128:131], v[186:189], v[190:193], v[128:131]
	s_waitcnt lgkmcnt(2)
	v_mfma_f32_16x16x32_bf16 v[124:127], v[160:163], v[194:197], v[124:127]
	ds_read_b128 v[190:193], v175 offset:8192
	v_mfma_f32_16x16x32_bf16 v[120:123], v[164:167], v[194:197], v[120:123]
	v_mfma_f32_16x16x32_bf16 v[116:119], v[182:185], v[194:197], v[116:119]
	v_mfma_f32_16x16x32_bf16 v[112:115], v[186:189], v[194:197], v[112:115]
	s_waitcnt lgkmcnt(2)
	v_mfma_f32_16x16x32_bf16 v[108:111], v[160:163], v[168:171], v[108:111]
	ds_read_b128 v[194:197], v175 offset:10240
	buffer_load_dwordx4 v[12:15], v173, s[8:11], s5 offen
	s_waitcnt vmcnt(10)
	v_cvt_pk_bf16_f32 v31, v30, v31
	v_cvt_pk_bf16_f32 v30, v28, v29
	v_mfma_f32_16x16x32_bf16 v[104:107], v[164:167], v[168:171], v[104:107]
	ds_write_b64 v174, v[30:31] offset:43520
	v_mfma_f32_16x16x32_bf16 v[100:103], v[182:185], v[168:171], v[100:103]
	v_mfma_f32_16x16x32_bf16 v[96:99], v[186:189], v[168:171], v[96:99]
	s_add_i32 s20, s1, 0xfff40000
	s_waitcnt lgkmcnt(2)
	v_mfma_f32_16x16x32_bf16 v[92:95], v[160:163], v[190:193], v[92:95]
	ds_read_b128 v[168:171], v175 offset:12288
	v_mfma_f32_16x16x32_bf16 v[88:91], v[164:167], v[190:193], v[88:91]
	v_mfma_f32_16x16x32_bf16 v[84:87], v[182:185], v[190:193], v[84:87]
	v_mfma_f32_16x16x32_bf16 v[80:83], v[186:189], v[190:193], v[80:83]
	s_waitcnt lgkmcnt(2)
	v_mfma_f32_16x16x32_bf16 v[76:79], v[160:163], v[194:197], v[76:79]
	ds_read_b128 v[190:193], v175 offset:14336
	v_cvt_pk_bf16_f32 v7, v6, v7
	v_cvt_pk_bf16_f32 v6, v4, v5
	v_mfma_f32_16x16x32_bf16 v[72:75], v[164:167], v[194:197], v[72:75]
	ds_write_b64 v174, v[6:7] offset:52224
	v_mfma_f32_16x16x32_bf16 v[68:71], v[182:185], v[194:197], v[68:71]
	v_mfma_f32_16x16x32_bf16 v[64:67], v[186:189], v[194:197], v[64:67]
	s_add_i32 s21, s1, 0xfff60000
	buffer_load_dwordx4 v[28:31], v173, s[8:11], s20 offen
	s_waitcnt lgkmcnt(2)
	v_mfma_f32_16x16x32_bf16 v[60:63], v[160:163], v[168:171], v[60:63]
	ds_read_b128 v[194:197], v175 offset:1024
	v_mfma_f32_16x16x32_bf16 v[56:59], v[164:167], v[168:171], v[56:59]
	v_mfma_f32_16x16x32_bf16 v[52:55], v[182:185], v[168:171], v[52:55]
	v_mfma_f32_16x16x32_bf16 v[48:51], v[186:189], v[168:171], v[48:51]
	s_waitcnt lgkmcnt(2)
	v_mfma_f32_16x16x32_bf16 v[44:47], v[160:163], v[190:193], v[44:47]
	ds_read_b128 v[160:163], v175 offset:3072
	buffer_load_dwordx4 v[4:7], v173, s[8:11], s21 offen
	s_waitcnt vmcnt(11)
	v_cvt_pk_bf16_f32 v27, v26, v27
	v_cvt_pk_bf16_f32 v26, v24, v25
	v_mfma_f32_16x16x32_bf16 v[40:43], v[164:167], v[190:193], v[40:43]
	ds_read_b64_tr_b16 v[244:245], v178 offset:17408
	ds_read_b64_tr_b16 v[248:249], v178 offset:17440
	ds_read_b64_tr_b16 v[198:199], v178 offset:17472
	ds_read_b64_tr_b16 v[202:203], v178 offset:17504
	ds_read_b64_tr_b16 v[246:247], v179 offset:17408
	ds_read_b64_tr_b16 v[250:251], v179 offset:17440
	ds_read_b64_tr_b16 v[200:201], v179 offset:17472
	ds_read_b64_tr_b16 v[204:205], v179 offset:17504
	ds_write_b64 v174, v[26:27] offset:60928
	v_mfma_f32_16x16x32_bf16 v[36:39], v[182:185], v[190:193], v[36:39]
	v_mfma_f32_16x16x32_bf16 v[32:35], v[186:189], v[190:193], v[32:35]
	s_add_i32 s22, s1, 0xfff80000
	s_waitcnt lgkmcnt(4)
	v_mfma_f32_16x16x32_bf16 v[156:159], v[244:247], v[194:197], v[156:159]
	ds_read_b128 v[182:185], v175 offset:5120
	s_waitcnt lgkmcnt(4)
	v_mfma_f32_16x16x32_bf16 v[152:155], v[248:251], v[194:197], v[152:155]
	s_waitcnt lgkmcnt(3)
	v_mfma_f32_16x16x32_bf16 v[148:151], v[198:201], v[194:197], v[148:151]
	s_waitcnt lgkmcnt(2)
	v_mfma_f32_16x16x32_bf16 v[144:147], v[202:205], v[194:197], v[144:147]
	v_mfma_f32_16x16x32_bf16 v[140:143], v[244:247], v[160:163], v[140:143]
	ds_read_b128 v[186:189], v175 offset:7168
	buffer_load_dwordx4 v[24:27], v173, s[8:11], s22 offen
	s_waitcnt vmcnt(11)
; #define G_ENDTILE(VM) do { asm volatile("s_waitcnt vmcnt(" #VM ")" ::: "memory"); \
;         asm volatile("s_waitcnt lgkmcnt(0)" ::: "memory"); __builtin_amdgcn_s_barrier(); asm volatile("" ::: "memory"); } while (0)
;     ...
;         for (int t = 0; t < nt - 2; t += 2) {
;             G_TILE(G_A0, G_B0, true, G_B1, G_A1, t + 1, true, t + 2, (void)0);
;             G_ENDTILE(8);
;             G_TILE(G_A1, G_B1, true, G_B0, G_A0, t + 2, true, t + 3, (void)0);
;             G_ENDTILE(8);
	v_cvt_pk_bf16_f32 v23, v22, v23
	v_cvt_pk_bf16_f32 v22, v20, v21
	v_mfma_f32_16x16x32_bf16 v[136:139], v[248:251], v[160:163], v[136:139]
	ds_write_b64 v174, v[22:23] offset:35072
	v_mfma_f32_16x16x32_bf16 v[132:135], v[198:201], v[160:163], v[132:135]
	v_mfma_f32_16x16x32_bf16 v[128:131], v[202:205], v[160:163], v[128:131]
	s_waitcnt lgkmcnt(2)
	v_mfma_f32_16x16x32_bf16 v[124:127], v[244:247], v[182:185], v[124:127]
	ds_read_b128 v[160:163], v175 offset:9216
	v_mfma_f32_16x16x32_bf16 v[120:123], v[248:251], v[182:185], v[120:123]
	v_mfma_f32_16x16x32_bf16 v[116:119], v[198:201], v[182:185], v[116:119]
	v_mfma_f32_16x16x32_bf16 v[112:115], v[202:205], v[182:185], v[112:115]
	s_waitcnt lgkmcnt(2)
	v_mfma_f32_16x16x32_bf16 v[108:111], v[244:247], v[186:189], v[108:111]
	ds_read_b128 v[182:185], v175 offset:11264
	buffer_load_dwordx4 v[20:23], v173, s[12:15], s5 offen
	s_waitcnt vmcnt(10)
	v_cvt_pk_bf16_f32 v11, v10, v11
	v_cvt_pk_bf16_f32 v10, v8, v9
	v_mfma_f32_16x16x32_bf16 v[104:107], v[248:251], v[186:189], v[104:107]
	ds_write_b64 v174, v[10:11] offset:43776
	v_mfma_f32_16x16x32_bf16 v[100:103], v[198:201], v[186:189], v[100:103]
	v_mfma_f32_16x16x32_bf16 v[96:99], v[202:205], v[186:189], v[96:99]
	s_waitcnt lgkmcnt(2)
	v_mfma_f32_16x16x32_bf16 v[92:95], v[244:247], v[160:163], v[92:95]
	ds_read_b128 v[186:189], v175 offset:13312
	v_mfma_f32_16x16x32_bf16 v[88:91], v[248:251], v[160:163], v[88:91]
	v_mfma_f32_16x16x32_bf16 v[84:87], v[198:201], v[160:163], v[84:87]
	v_mfma_f32_16x16x32_bf16 v[80:83], v[202:205], v[160:163], v[80:83]
	s_waitcnt lgkmcnt(2)
	v_mfma_f32_16x16x32_bf16 v[76:79], v[244:247], v[182:185], v[76:79]
	ds_read_b128 v[252:255], v175 offset:15360
	v_cvt_pk_bf16_f32 v3, v2, v3
	v_cvt_pk_bf16_f32 v2, v0, v1
	v_mfma_f32_16x16x32_bf16 v[72:75], v[248:251], v[182:185], v[72:75]
	ds_write_b64 v174, v[2:3] offset:52480
	v_mfma_f32_16x16x32_bf16 v[68:71], v[198:201], v[182:185], v[68:71]
	v_mfma_f32_16x16x32_bf16 v[64:67], v[202:205], v[182:185], v[64:67]
	buffer_load_dwordx4 v[8:11], v173, s[12:15], s20 offen
	s_waitcnt lgkmcnt(2)
	v_mfma_f32_16x16x32_bf16 v[60:63], v[244:247], v[186:189], v[60:63]
	v_mfma_f32_16x16x32_bf16 v[56:59], v[248:251], v[186:189], v[56:59]
	v_mfma_f32_16x16x32_bf16 v[52:55], v[198:201], v[186:189], v[52:55]
	v_mfma_f32_16x16x32_bf16 v[48:51], v[202:205], v[186:189], v[48:51]
	s_waitcnt lgkmcnt(1)
	buffer_load_dwordx4 v[0:3], v173, s[12:15], s21 offen
	s_waitcnt vmcnt(11)
	v_cvt_pk_bf16_f32 v19, v18, v19
	v_cvt_pk_bf16_f32 v18, v16, v17
	ds_write_b64 v174, v[18:19] offset:61184
	buffer_load_dwordx4 v[16:19], v173, s[12:15], s22 offen
	s_waitcnt vmcnt(8)
	s_mov_b32 m0, s45
	s_waitcnt lgkmcnt(0)
	s_barrier
	ds_read_b64_tr_b16 v[160:161], v178 offset:34816
	ds_read_b64_tr_b16 v[162:163], v179 offset:34816
	ds_read_b64_tr_b16 v[166:167], v179 offset:34848
	ds_read_b128 v[168:171], v175 offset:32768
	ds_read_b64_tr_b16 v[164:165], v178 offset:34848
	ds_read_b64_tr_b16 v[182:183], v178 offset:34880
	ds_read_b64_tr_b16 v[186:187], v178 offset:34912
	ds_read_b64_tr_b16 v[184:185], v179 offset:34880
	ds_read_b64_tr_b16 v[188:189], v179 offset:34912
	ds_read_b128 v[190:193], v175 offset:34816
	ds_read_b128 v[194:197], v175 offset:36864
	buffer_load_dwordx4 v176, s[16:19], s4 offen lds
	s_mov_b32 m0, s53
	v_mfma_f32_16x16x32_bf16 v[44:47], v[244:247], v[252:255], v[44:47]
	v_mfma_f32_16x16x32_bf16 v[40:43], v[248:251], v[252:255], v[40:43]
	v_mfma_f32_16x16x32_bf16 v[36:39], v[198:201], v[252:255], v[36:39]
	v_mfma_f32_16x16x32_bf16 v[32:35], v[202:205], v[252:255], v[32:35]
	s_waitcnt lgkmcnt(7)
	v_mfma_f32_16x16x32_bf16 v[156:159], v[160:163], v[168:171], v[156:159]
	buffer_load_dwordx4 v177, s[16:19], s4 offen lds
	s_add_i32 s5, s1, 0xfffa0000
	s_waitcnt lgkmcnt(6)
	v_mfma_f32_16x16x32_bf16 v[152:155], v[164:167], v[168:171], v[152:155]
	s_waitcnt lgkmcnt(3)
	v_mfma_f32_16x16x32_bf16 v[148:151], v[182:185], v[168:171], v[148:151]
	s_waitcnt lgkmcnt(2)
	v_mfma_f32_16x16x32_bf16 v[144:147], v[186:189], v[168:171], v[144:147]
	s_waitcnt lgkmcnt(1)
	v_mfma_f32_16x16x32_bf16 v[140:143], v[160:163], v[190:193], v[140:143]
	s_mov_b32 m0, s54
	s_nop 0
	buffer_load_dwordx4 v180, s[16:19], s4 offen lds
	ds_read_b128 v[168:171], v175 offset:38912
	s_waitcnt vmcnt(10)
	v_cvt_pk_bf16_f32 v15, v14, v15
	v_cvt_pk_bf16_f32 v14, v12, v13
	v_mfma_f32_16x16x32_bf16 v[136:139], v[164:167], v[190:193], v[136:139]
	ds_write_b64 v174, v[14:15]
	v_mfma_f32_16x16x32_bf16 v[132:135], v[182:185], v[190:193], v[132:135]
	s_mov_b32 m0, s55
	s_nop 0
	buffer_load_dwordx4 v181, s[16:19], s4 offen lds
	v_mfma_f32_16x16x32_bf16 v[128:131], v[186:189], v[190:193], v[128:131]
	s_waitcnt lgkmcnt(2)
	v_mfma_f32_16x16x32_bf16 v[124:127], v[160:163], v[194:197], v[124:127]
	ds_read_b128 v[190:193], v175 offset:40960
	v_mfma_f32_16x16x32_bf16 v[120:123], v[164:167], v[194:197], v[120:123]
	v_mfma_f32_16x16x32_bf16 v[116:119], v[182:185], v[194:197], v[116:119]
	v_mfma_f32_16x16x32_bf16 v[112:115], v[186:189], v[194:197], v[112:115]
	s_waitcnt lgkmcnt(2)
	v_mfma_f32_16x16x32_bf16 v[108:111], v[160:163], v[168:171], v[108:111]
	ds_read_b128 v[194:197], v175 offset:43008
	buffer_load_dwordx4 v[12:15], v173, s[8:11], s5 offen
	s_waitcnt vmcnt(11)
	v_cvt_pk_bf16_f32 v31, v30, v31
	v_cvt_pk_bf16_f32 v30, v28, v29
	v_mfma_f32_16x16x32_bf16 v[104:107], v[164:167], v[168:171], v[104:107]
	ds_write_b64 v174, v[30:31] offset:8704
	v_mfma_f32_16x16x32_bf16 v[100:103], v[182:185], v[168:171], v[100:103]
	v_mfma_f32_16x16x32_bf16 v[96:99], v[186:189], v[168:171], v[96:99]
	s_add_i32 s20, s1, 0xfffc0000
	s_waitcnt lgkmcnt(2)
; #define G_ENDTILE(VM) do { asm volatile("s_waitcnt vmcnt(" #VM ")" ::: "memory"); \
;         asm volatile("s_waitcnt lgkmcnt(0)" ::: "memory"); __builtin_amdgcn_s_barrier(); asm volatile("" ::: "memory"); } while (0)
;     ...
;         for (int t = 0; t < nt - 2; t += 2) {
;             G_TILE(G_A0, G_B0, true, G_B1, G_A1, t + 1, true, t + 2, (void)0);
;             G_ENDTILE(8);
;             G_TILE(G_A1, G_B1, true, G_B0, G_A0, t + 2, true, t + 3, (void)0);
;             G_ENDTILE(8);
;         }
	v_mfma_f32_16x16x32_bf16 v[92:95], v[160:163], v[190:193], v[92:95]
	ds_read_b128 v[168:171], v175 offset:45056
	v_mfma_f32_16x16x32_bf16 v[88:91], v[164:167], v[190:193], v[88:91]
	v_mfma_f32_16x16x32_bf16 v[84:87], v[182:185], v[190:193], v[84:87]
	v_mfma_f32_16x16x32_bf16 v[80:83], v[186:189], v[190:193], v[80:83]
	s_waitcnt lgkmcnt(2)
	v_mfma_f32_16x16x32_bf16 v[76:79], v[160:163], v[194:197], v[76:79]
	ds_read_b128 v[190:193], v175 offset:47104
	buffer_load_dwordx4 v[28:31], v173, s[8:11], s20 offen
	s_waitcnt vmcnt(11)
	v_cvt_pk_bf16_f32 v7, v6, v7
	v_cvt_pk_bf16_f32 v6, v4, v5
	v_mfma_f32_16x16x32_bf16 v[72:75], v[164:167], v[194:197], v[72:75]
	ds_write_b64 v174, v[6:7] offset:17408
	v_mfma_f32_16x16x32_bf16 v[68:71], v[182:185], v[194:197], v[68:71]
	v_mfma_f32_16x16x32_bf16 v[64:67], v[186:189], v[194:197], v[64:67]
	s_add_i32 s21, s1, 0xfffe0000
	s_waitcnt lgkmcnt(2)
	v_mfma_f32_16x16x32_bf16 v[60:63], v[160:163], v[168:171], v[60:63]
	ds_read_b128 v[194:197], v175 offset:33792
	v_mfma_f32_16x16x32_bf16 v[56:59], v[164:167], v[168:171], v[56:59]
	v_mfma_f32_16x16x32_bf16 v[52:55], v[182:185], v[168:171], v[52:55]
	v_mfma_f32_16x16x32_bf16 v[48:51], v[186:189], v[168:171], v[48:51]
	s_waitcnt lgkmcnt(2)
	v_mfma_f32_16x16x32_bf16 v[44:47], v[160:163], v[190:193], v[44:47]
	ds_read_b128 v[160:163], v175 offset:35840
	buffer_load_dwordx4 v[4:7], v173, s[8:11], s21 offen
	s_waitcnt vmcnt(11)
	v_cvt_pk_bf16_f32 v27, v26, v27
	v_cvt_pk_bf16_f32 v26, v24, v25
	v_mfma_f32_16x16x32_bf16 v[40:43], v[164:167], v[190:193], v[40:43]
	ds_read_b64_tr_b16 v[244:245], v178 offset:52224
	ds_read_b64_tr_b16 v[248:249], v178 offset:52256
	ds_read_b64_tr_b16 v[198:199], v178 offset:52288
	ds_read_b64_tr_b16 v[202:203], v178 offset:52320
	ds_read_b64_tr_b16 v[246:247], v179 offset:52224
	ds_read_b64_tr_b16 v[250:251], v179 offset:52256
	ds_read_b64_tr_b16 v[200:201], v179 offset:52288
	ds_read_b64_tr_b16 v[204:205], v179 offset:52320
	ds_write_b64 v174, v[26:27] offset:26112
	v_mfma_f32_16x16x32_bf16 v[36:39], v[182:185], v[190:193], v[36:39]
	v_mfma_f32_16x16x32_bf16 v[32:35], v[186:189], v[190:193], v[32:35]
	s_waitcnt lgkmcnt(4)
	v_mfma_f32_16x16x32_bf16 v[156:159], v[244:247], v[194:197], v[156:159]
	ds_read_b128 v[182:185], v175 offset:37888
	s_waitcnt lgkmcnt(4)
	v_mfma_f32_16x16x32_bf16 v[152:155], v[248:251], v[194:197], v[152:155]
	s_waitcnt lgkmcnt(3)
	v_mfma_f32_16x16x32_bf16 v[148:151], v[198:201], v[194:197], v[148:151]
	s_waitcnt lgkmcnt(2)
	v_mfma_f32_16x16x32_bf16 v[144:147], v[202:205], v[194:197], v[144:147]
	v_mfma_f32_16x16x32_bf16 v[140:143], v[244:247], v[160:163], v[140:143]
	ds_read_b128 v[186:189], v175 offset:39936
	buffer_load_dwordx4 v[24:27], v173, s[8:11], s1 offen
	s_waitcnt vmcnt(11)
	v_cvt_pk_bf16_f32 v23, v22, v23
	v_cvt_pk_bf16_f32 v22, v20, v21
	v_mfma_f32_16x16x32_bf16 v[136:139], v[248:251], v[160:163], v[136:139]
	ds_write_b64 v174, v[22:23] offset:256
	v_mfma_f32_16x16x32_bf16 v[132:135], v[198:201], v[160:163], v[132:135]
	v_mfma_f32_16x16x32_bf16 v[128:131], v[202:205], v[160:163], v[128:131]
	s_waitcnt lgkmcnt(2)
	v_mfma_f32_16x16x32_bf16 v[124:127], v[244:247], v[182:185], v[124:127]
	ds_read_b128 v[160:163], v175 offset:41984
	v_mfma_f32_16x16x32_bf16 v[120:123], v[248:251], v[182:185], v[120:123]
	v_mfma_f32_16x16x32_bf16 v[116:119], v[198:201], v[182:185], v[116:119]
	v_mfma_f32_16x16x32_bf16 v[112:115], v[202:205], v[182:185], v[112:115]
	s_waitcnt lgkmcnt(2)
	v_mfma_f32_16x16x32_bf16 v[108:111], v[244:247], v[186:189], v[108:111]
	ds_read_b128 v[182:185], v175 offset:44032
	buffer_load_dwordx4 v[20:23], v173, s[12:15], s5 offen
	s_waitcnt vmcnt(11)
	v_cvt_pk_bf16_f32 v11, v10, v11
	v_cvt_pk_bf16_f32 v10, v8, v9
	v_mfma_f32_16x16x32_bf16 v[104:107], v[248:251], v[186:189], v[104:107]
	ds_write_b64 v174, v[10:11] offset:8960
	v_mfma_f32_16x16x32_bf16 v[100:103], v[198:201], v[186:189], v[100:103]
	v_mfma_f32_16x16x32_bf16 v[96:99], v[202:205], v[186:189], v[96:99]
	s_waitcnt lgkmcnt(2)
	v_mfma_f32_16x16x32_bf16 v[92:95], v[244:247], v[160:163], v[92:95]
	ds_read_b128 v[186:189], v175 offset:46080
	v_mfma_f32_16x16x32_bf16 v[88:91], v[248:251], v[160:163], v[88:91]
	v_mfma_f32_16x16x32_bf16 v[84:87], v[198:201], v[160:163], v[84:87]
	v_mfma_f32_16x16x32_bf16 v[80:83], v[202:205], v[160:163], v[80:83]
	s_waitcnt lgkmcnt(2)
	v_mfma_f32_16x16x32_bf16 v[76:79], v[244:247], v[182:185], v[76:79]
	ds_read_b128 v[252:255], v175 offset:48128
	buffer_load_dwordx4 v[8:11], v173, s[12:15], s20 offen
	s_waitcnt vmcnt(11)
	v_cvt_pk_bf16_f32 v3, v2, v3
	v_cvt_pk_bf16_f32 v2, v0, v1
	v_mfma_f32_16x16x32_bf16 v[72:75], v[248:251], v[182:185], v[72:75]
	ds_write_b64 v174, v[2:3] offset:17664
	v_mfma_f32_16x16x32_bf16 v[68:71], v[198:201], v[182:185], v[68:71]
	v_mfma_f32_16x16x32_bf16 v[64:67], v[202:205], v[182:185], v[64:67]
	s_waitcnt lgkmcnt(2)
	v_mfma_f32_16x16x32_bf16 v[60:63], v[244:247], v[186:189], v[60:63]
	v_mfma_f32_16x16x32_bf16 v[56:59], v[248:251], v[186:189], v[56:59]
	v_mfma_f32_16x16x32_bf16 v[52:55], v[198:201], v[186:189], v[52:55]
	v_mfma_f32_16x16x32_bf16 v[48:51], v[202:205], v[186:189], v[48:51]
	s_waitcnt lgkmcnt(1)
	buffer_load_dwordx4 v[0:3], v173, s[12:15], s21 offen
	s_waitcnt vmcnt(11)
	v_cvt_pk_bf16_f32 v19, v18, v19
	v_cvt_pk_bf16_f32 v18, v16, v17
	ds_write_b64 v174, v[18:19] offset:26368
	buffer_load_dwordx4 v[16:19], v173, s[12:15], s1 offen
	s_waitcnt vmcnt(8)
	s_waitcnt lgkmcnt(0)
	s_barrier
	s_add_i32 s0, s0, 2
	s_add_i32 s1, s1, 0x100000
	s_addk_i32 s4, 0x100
	s_cmp_ge_i32 s0, s60
	s_cbranch_scc0 .LBB0_1038
	v_mfma_f32_16x16x32_bf16 v[44:47], v[244:247], v[252:255], v[44:47]
	v_mfma_f32_16x16x32_bf16 v[40:43], v[248:251], v[252:255], v[40:43]
	v_mfma_f32_16x16x32_bf16 v[36:39], v[198:201], v[252:255], v[36:39]
	v_mfma_f32_16x16x32_bf16 v[32:35], v[202:205], v[252:255], v[32:35]
	s_branch .LBB0_1040
